# speedup vs baseline: 1.0013x; 1.0013x over previous
.Lc_go:
	s_cmp_eq_u32 s45, 0
	s_cbranch_scc0 .Lc_par1
	ds_read2_b64 v[48:51], v32 offset0:0 offset1:202
	ds_read2_b64 v[52:55], v32 offset0:1 offset1:203
	ds_read_b128 v[120:123], v33 offset:0
	ds_read2_b64 v[10:13], v34 offset0:0 offset1:202
	ds_read2_b64 v[56:59], v32 offset0:2 offset1:204
	ds_read2_b64 v[60:63], v32 offset0:3 offset1:205
	ds_read_b128 v[124:127], v33 offset:16
	ds_read2_b64 v[64:67], v32 offset0:4 offset1:206
	ds_read2_b64 v[68:71], v32 offset0:5 offset1:207
	ds_read_b128 v[128:131], v33 offset:32
	ds_read2_b64 v[72:75], v32 offset0:6 offset1:208
	s_mov_b32 s70, 0
	s_mov_b32 s71, 0
.Lc0_loop:
	s_waitcnt lgkmcnt(4)
	v_pk_fma_f16 v6, v2, v120, v121 op_sel:[0,0,0] op_sel_hi:[1,0,0] neg_lo:[1,0,0] neg_hi:[1,0,0]
	v_pk_fma_f16 v7, v3, v120, v121 op_sel:[0,0,0] op_sel_hi:[1,0,0] neg_lo:[1,0,0] neg_hi:[1,0,0]
	v_pk_fma_f16 v8, v4, v120, v121 op_sel:[0,0,0] op_sel_hi:[1,0,0] neg_lo:[1,0,0] neg_hi:[1,0,0]
	v_pk_fma_f16 v9, v5, v120, v121 op_sel:[0,0,0] op_sel_hi:[1,0,0] neg_lo:[1,0,0] neg_hi:[1,0,0]
	v_mfma_f32_16x16x32_f16 v[18:21], v[10:13], v[2:5], 0
	ds_read2_b64 v[76:79], v32 offset0:7 offset1:209
	ds_read_b128 v[132:135], v33 offset:48
	ds_read_b32 v37, v36 offset:4
	ds_read_b32 v38, v36 offset:68
	v_pk_fma_f16 v2, v48, v6, v2
	v_pk_fma_f16 v3, v49, v7, v3
	v_pk_fma_f16 v4, v50, v8, v4
	v_pk_fma_f16 v5, v51, v9, v5
	v_cndmask_b32_e64 v29, v29, v25, s[66:67]
	v_cvt_pk_f16_f32 v30, v26, v27
	v_cvt_pk_f16_f32 v31, v28, v29
	ds_write_b16 v39, v30 offset:0
	ds_write_b16_d16_hi v39, v30 offset:64
	ds_write_b16 v39, v31 offset:128
	ds_write_b16_d16_hi v39, v31 offset:192
	s_mov_b64 exec, 1
	ds_add_u32 v36, v44 offset:124
	s_mov_b64 exec, -1
	v_pk_fma_f16 v6, v2, v122, v123 op_sel:[0,0,0] op_sel_hi:[1,0,0] neg_lo:[1,0,0] neg_hi:[1,0,0]
	v_pk_fma_f16 v7, v3, v122, v123 op_sel:[0,0,0] op_sel_hi:[1,0,0] neg_lo:[1,0,0] neg_hi:[1,0,0]
	v_pk_fma_f16 v8, v4, v122, v123 op_sel:[0,0,0] op_sel_hi:[1,0,0] neg_lo:[1,0,0] neg_hi:[1,0,0]
	v_pk_fma_f16 v9, v5, v122, v123 op_sel:[0,0,0] op_sel_hi:[1,0,0] neg_lo:[1,0,0] neg_hi:[1,0,0]
	v_mfma_f32_16x16x32_f16 v[22:25], v[10:13], v[2:5], 0
	ds_read2_b64 v[80:83], v32 offset0:8 offset1:210
	v_pk_fma_f16 v2, v52, v6, v2
	v_pk_fma_f16 v3, v53, v7, v3
	v_pk_fma_f16 v4, v54, v8, v4
	v_pk_fma_f16 v5, v55, v9, v5
	v_cndmask_b32_e64 v26, v26, v18, s[60:61]
	v_pk_fma_f16 v6, v2, v124, v125 op_sel:[0,0,0] op_sel_hi:[1,0,0] neg_lo:[1,0,0] neg_hi:[1,0,0]
	v_pk_fma_f16 v7, v3, v124, v125 op_sel:[0,0,0] op_sel_hi:[1,0,0] neg_lo:[1,0,0] neg_hi:[1,0,0]
	v_pk_fma_f16 v8, v4, v124, v125 op_sel:[0,0,0] op_sel_hi:[1,0,0] neg_lo:[1,0,0] neg_hi:[1,0,0]
	v_pk_fma_f16 v9, v5, v124, v125 op_sel:[0,0,0] op_sel_hi:[1,0,0] neg_lo:[1,0,0] neg_hi:[1,0,0]
	v_mfma_f32_16x16x32_f16 v[18:21], v[10:13], v[2:5], 0
	ds_read2_b64 v[84:87], v32 offset0:9 offset1:211
	ds_read_b128 v[136:139], v33 offset:64
	v_pk_fma_f16 v2, v56, v6, v2
	v_pk_fma_f16 v3, v57, v7, v3
	v_pk_fma_f16 v4, v58, v8, v4
	v_pk_fma_f16 v5, v59, v9, v5
	v_cndmask_b32_e64 v27, v27, v23, s[60:61]
	v_pk_fma_f16 v6, v2, v126, v127 op_sel:[0,0,0] op_sel_hi:[1,0,0] neg_lo:[1,0,0] neg_hi:[1,0,0]
	v_pk_fma_f16 v7, v3, v126, v127 op_sel:[0,0,0] op_sel_hi:[1,0,0] neg_lo:[1,0,0] neg_hi:[1,0,0]
	v_pk_fma_f16 v8, v4, v126, v127 op_sel:[0,0,0] op_sel_hi:[1,0,0] neg_lo:[1,0,0] neg_hi:[1,0,0]
	v_pk_fma_f16 v9, v5, v126, v127 op_sel:[0,0,0] op_sel_hi:[1,0,0] neg_lo:[1,0,0] neg_hi:[1,0,0]
	v_mfma_f32_16x16x32_f16 v[22:25], v[10:13], v[2:5], 0
	ds_read2_b64 v[88:91], v32 offset0:10 offset1:212
	v_pk_fma_f16 v2, v60, v6, v2
	v_pk_fma_f16 v3, v61, v7, v3
	v_pk_fma_f16 v4, v62, v8, v4
	v_pk_fma_f16 v5, v63, v9, v5
	v_cndmask_b32_e64 v28, v28, v20, s[60:61]
	s_waitcnt lgkmcnt(11)
	v_pk_fma_f16 v6, v2, v128, v129 op_sel:[0,0,0] op_sel_hi:[1,0,0] neg_lo:[1,0,0] neg_hi:[1,0,0]
	v_pk_fma_f16 v7, v3, v128, v129 op_sel:[0,0,0] op_sel_hi:[1,0,0] neg_lo:[1,0,0] neg_hi:[1,0,0]
	v_pk_fma_f16 v8, v4, v128, v129 op_sel:[0,0,0] op_sel_hi:[1,0,0] neg_lo:[1,0,0] neg_hi:[1,0,0]
	v_pk_fma_f16 v9, v5, v128, v129 op_sel:[0,0,0] op_sel_hi:[1,0,0] neg_lo:[1,0,0] neg_hi:[1,0,0]
	v_mfma_f32_16x16x32_f16 v[18:21], v[10:13], v[2:5], 0
	ds_read2_b64 v[92:95], v32 offset0:11 offset1:213
	ds_read_b128 v[140:143], v33 offset:80
	v_pk_fma_f16 v2, v64, v6, v2
	v_pk_fma_f16 v3, v65, v7, v3
	v_pk_fma_f16 v4, v66, v8, v4
	v_pk_fma_f16 v5, v67, v9, v5
	v_cndmask_b32_e64 v29, v29, v25, s[60:61]
	v_pk_fma_f16 v6, v2, v130, v131 op_sel:[0,0,0] op_sel_hi:[1,0,0] neg_lo:[1,0,0] neg_hi:[1,0,0]
	v_pk_fma_f16 v7, v3, v130, v131 op_sel:[0,0,0] op_sel_hi:[1,0,0] neg_lo:[1,0,0] neg_hi:[1,0,0]
	v_pk_fma_f16 v8, v4, v130, v131 op_sel:[0,0,0] op_sel_hi:[1,0,0] neg_lo:[1,0,0] neg_hi:[1,0,0]
	v_pk_fma_f16 v9, v5, v130, v131 op_sel:[0,0,0] op_sel_hi:[1,0,0] neg_lo:[1,0,0] neg_hi:[1,0,0]
	v_mfma_f32_16x16x32_f16 v[22:25], v[10:13], v[2:5], 0
	ds_read2_b64 v[96:99], v32 offset0:12 offset1:214
	v_pk_fma_f16 v2, v68, v6, v2
	v_pk_fma_f16 v3, v69, v7, v3
	v_pk_fma_f16 v4, v70, v8, v4
	v_pk_fma_f16 v5, v71, v9, v5
	v_cndmask_b32_e64 v26, v26, v18, s[62:63]
	v_pk_fma_f16 v6, v2, v132, v133 op_sel:[0,0,0] op_sel_hi:[1,0,0] neg_lo:[1,0,0] neg_hi:[1,0,0]
	v_pk_fma_f16 v7, v3, v132, v133 op_sel:[0,0,0] op_sel_hi:[1,0,0] neg_lo:[1,0,0] neg_hi:[1,0,0]
	v_pk_fma_f16 v8, v4, v132, v133 op_sel:[0,0,0] op_sel_hi:[1,0,0] neg_lo:[1,0,0] neg_hi:[1,0,0]
	v_pk_fma_f16 v9, v5, v132, v133 op_sel:[0,0,0] op_sel_hi:[1,0,0] neg_lo:[1,0,0] neg_hi:[1,0,0]
	v_mfma_f32_16x16x32_f16 v[18:21], v[10:13], v[2:5], 0
	ds_read2_b64 v[100:103], v32 offset0:13 offset1:215
	ds_read_b128 v[144:147], v33 offset:96
	v_pk_fma_f16 v2, v72, v6, v2
	v_pk_fma_f16 v3, v73, v7, v3
	v_pk_fma_f16 v4, v74, v8, v4
	v_pk_fma_f16 v5, v75, v9, v5
	v_cndmask_b32_e64 v27, v27, v23, s[62:63]
	v_pk_fma_f16 v6, v2, v134, v135 op_sel:[0,0,0] op_sel_hi:[1,0,0] neg_lo:[1,0,0] neg_hi:[1,0,0]
	v_pk_fma_f16 v7, v3, v134, v135 op_sel:[0,0,0] op_sel_hi:[1,0,0] neg_lo:[1,0,0] neg_hi:[1,0,0]
	v_pk_fma_f16 v8, v4, v134, v135 op_sel:[0,0,0] op_sel_hi:[1,0,0] neg_lo:[1,0,0] neg_hi:[1,0,0]
	v_pk_fma_f16 v9, v5, v134, v135 op_sel:[0,0,0] op_sel_hi:[1,0,0] neg_lo:[1,0,0] neg_hi:[1,0,0]
	v_mfma_f32_16x16x32_f16 v[22:25], v[10:13], v[2:5], 0
	ds_read2_b64 v[104:107], v32 offset0:14 offset1:216
	v_pk_fma_f16 v2, v76, v6, v2
	v_pk_fma_f16 v3, v77, v7, v3
	v_pk_fma_f16 v4, v78, v8, v4
	v_pk_fma_f16 v5, v79, v9, v5
	v_cndmask_b32_e64 v28, v28, v20, s[62:63]
	s_waitcnt lgkmcnt(4)
	v_pk_fma_f16 v6, v2, v136, v137 op_sel:[0,0,0] op_sel_hi:[1,0,0] neg_lo:[1,0,0] neg_hi:[1,0,0]
	v_pk_fma_f16 v7, v3, v136, v137 op_sel:[0,0,0] op_sel_hi:[1,0,0] neg_lo:[1,0,0] neg_hi:[1,0,0]
	v_pk_fma_f16 v8, v4, v136, v137 op_sel:[0,0,0] op_sel_hi:[1,0,0] neg_lo:[1,0,0] neg_hi:[1,0,0]
	v_pk_fma_f16 v9, v5, v136, v137 op_sel:[0,0,0] op_sel_hi:[1,0,0] neg_lo:[1,0,0] neg_hi:[1,0,0]
	v_mfma_f32_16x16x32_f16 v[18:21], v[10:13], v[2:5], 0
	ds_read2_b64 v[108:111], v32 offset0:15 offset1:217
	ds_read_b128 v[148:151], v33 offset:112
	v_pk_fma_f16 v2, v80, v6, v2
	v_pk_fma_f16 v3, v81, v7, v3
	v_pk_fma_f16 v4, v82, v8, v4
	v_pk_fma_f16 v5, v83, v9, v5
	v_cndmask_b32_e64 v29, v29, v25, s[62:63]
	v_readfirstlane_b32 s4, v37
	v_readfirstlane_b32 s5, v38
	s_and_b32 s4, s4, s5
	s_cbranch_scc0 .Lc0_slow0
.Lc0_back0:
	v_pk_fma_f16 v6, v2, v138, v139 op_sel:[0,0,0] op_sel_hi:[1,0,0] neg_lo:[1,0,0] neg_hi:[1,0,0]
	v_pk_fma_f16 v7, v3, v138, v139 op_sel:[0,0,0] op_sel_hi:[1,0,0] neg_lo:[1,0,0] neg_hi:[1,0,0]
	v_pk_fma_f16 v8, v4, v138, v139 op_sel:[0,0,0] op_sel_hi:[1,0,0] neg_lo:[1,0,0] neg_hi:[1,0,0]
	v_pk_fma_f16 v9, v5, v138, v139 op_sel:[0,0,0] op_sel_hi:[1,0,0] neg_lo:[1,0,0] neg_hi:[1,0,0]
	v_mfma_f32_16x16x32_f16 v[22:25], v[10:13], v[2:5], 0
	ds_read2_b64 v[48:51], v32 offset0:16 offset1:218
	v_pk_fma_f16 v2, v84, v6, v2
	v_pk_fma_f16 v3, v85, v7, v3
	v_pk_fma_f16 v4, v86, v8, v4
	v_pk_fma_f16 v5, v87, v9, v5
	v_cndmask_b32_e64 v26, v26, v18, s[64:65]
	v_pk_fma_f16 v6, v2, v140, v141 op_sel:[0,0,0] op_sel_hi:[1,0,0] neg_lo:[1,0,0] neg_hi:[1,0,0]
	v_pk_fma_f16 v7, v3, v140, v141 op_sel:[0,0,0] op_sel_hi:[1,0,0] neg_lo:[1,0,0] neg_hi:[1,0,0]
	v_pk_fma_f16 v8, v4, v140, v141 op_sel:[0,0,0] op_sel_hi:[1,0,0] neg_lo:[1,0,0] neg_hi:[1,0,0]
	v_pk_fma_f16 v9, v5, v140, v141 op_sel:[0,0,0] op_sel_hi:[1,0,0] neg_lo:[1,0,0] neg_hi:[1,0,0]
	v_mfma_f32_16x16x32_f16 v[18:21], v[10:13], v[2:5], 0
	ds_read2_b64 v[52:55], v32 offset0:17 offset1:219
	ds_read_b128 v[120:123], v33 offset:128
	ds_read2_b64 v[14:17], v34 offset0:16 offset1:218
	v_pk_fma_f16 v2, v88, v6, v2
	v_pk_fma_f16 v3, v89, v7, v3
	v_pk_fma_f16 v4, v90, v8, v4
	v_pk_fma_f16 v5, v91, v9, v5
	v_cndmask_b32_e64 v27, v27, v23, s[64:65]
	v_pk_fma_f16 v6, v2, v142, v143 op_sel:[0,0,0] op_sel_hi:[1,0,0] neg_lo:[1,0,0] neg_hi:[1,0,0]
	v_pk_fma_f16 v7, v3, v142, v143 op_sel:[0,0,0] op_sel_hi:[1,0,0] neg_lo:[1,0,0] neg_hi:[1,0,0]
	v_pk_fma_f16 v8, v4, v142, v143 op_sel:[0,0,0] op_sel_hi:[1,0,0] neg_lo:[1,0,0] neg_hi:[1,0,0]
	v_pk_fma_f16 v9, v5, v142, v143 op_sel:[0,0,0] op_sel_hi:[1,0,0] neg_lo:[1,0,0] neg_hi:[1,0,0]
	v_mfma_f32_16x16x32_f16 v[22:25], v[10:13], v[2:5], 0
	ds_read2_b64 v[56:59], v32 offset0:18 offset1:220
	v_pk_fma_f16 v2, v92, v6, v2
	v_pk_fma_f16 v3, v93, v7, v3
	v_pk_fma_f16 v4, v94, v8, v4
	v_pk_fma_f16 v5, v95, v9, v5
	v_cndmask_b32_e64 v28, v28, v20, s[64:65]
	s_waitcnt lgkmcnt(5)
	v_pk_fma_f16 v6, v2, v144, v145 op_sel:[0,0,0] op_sel_hi:[1,0,0] neg_lo:[1,0,0] neg_hi:[1,0,0]
	v_pk_fma_f16 v7, v3, v144, v145 op_sel:[0,0,0] op_sel_hi:[1,0,0] neg_lo:[1,0,0] neg_hi:[1,0,0]
	v_pk_fma_f16 v8, v4, v144, v145 op_sel:[0,0,0] op_sel_hi:[1,0,0] neg_lo:[1,0,0] neg_hi:[1,0,0]
	v_pk_fma_f16 v9, v5, v144, v145 op_sel:[0,0,0] op_sel_hi:[1,0,0] neg_lo:[1,0,0] neg_hi:[1,0,0]
	v_mfma_f32_16x16x32_f16 v[18:21], v[10:13], v[2:5], 0
	ds_read2_b64 v[60:63], v32 offset0:19 offset1:221
	ds_read_b128 v[124:127], v33 offset:144
	v_pk_fma_f16 v2, v96, v6, v2
	v_pk_fma_f16 v3, v97, v7, v3
	v_pk_fma_f16 v4, v98, v8, v4
	v_pk_fma_f16 v5, v99, v9, v5
	v_cndmask_b32_e64 v29, v29, v25, s[64:65]
	v_pk_fma_f16 v6, v2, v146, v147 op_sel:[0,0,0] op_sel_hi:[1,0,0] neg_lo:[1,0,0] neg_hi:[1,0,0]
	v_pk_fma_f16 v7, v3, v146, v147 op_sel:[0,0,0] op_sel_hi:[1,0,0] neg_lo:[1,0,0] neg_hi:[1,0,0]
	v_pk_fma_f16 v8, v4, v146, v147 op_sel:[0,0,0] op_sel_hi:[1,0,0] neg_lo:[1,0,0] neg_hi:[1,0,0]
	v_pk_fma_f16 v9, v5, v146, v147 op_sel:[0,0,0] op_sel_hi:[1,0,0] neg_lo:[1,0,0] neg_hi:[1,0,0]
	v_mfma_f32_16x16x32_f16 v[22:25], v[10:13], v[2:5], 0
	ds_read2_b64 v[64:67], v32 offset0:20 offset1:222
	v_pk_fma_f16 v2, v100, v6, v2
	v_pk_fma_f16 v3, v101, v7, v3
	v_pk_fma_f16 v4, v102, v8, v4
	v_pk_fma_f16 v5, v103, v9, v5
	v_cndmask_b32_e64 v26, v26, v18, s[66:67]
	v_pk_fma_f16 v6, v2, v148, v149 op_sel:[0,0,0] op_sel_hi:[1,0,0] neg_lo:[1,0,0] neg_hi:[1,0,0]
	v_pk_fma_f16 v7, v3, v148, v149 op_sel:[0,0,0] op_sel_hi:[1,0,0] neg_lo:[1,0,0] neg_hi:[1,0,0]
	v_pk_fma_f16 v8, v4, v148, v149 op_sel:[0,0,0] op_sel_hi:[1,0,0] neg_lo:[1,0,0] neg_hi:[1,0,0]
	v_pk_fma_f16 v9, v5, v148, v149 op_sel:[0,0,0] op_sel_hi:[1,0,0] neg_lo:[1,0,0] neg_hi:[1,0,0]
	v_mfma_f32_16x16x32_f16 v[18:21], v[10:13], v[2:5], 0
	ds_read2_b64 v[68:71], v32 offset0:21 offset1:223
	ds_read_b128 v[128:131], v33 offset:160
	v_pk_fma_f16 v2, v104, v6, v2
	v_pk_fma_f16 v3, v105, v7, v3
	v_pk_fma_f16 v4, v106, v8, v4
	v_pk_fma_f16 v5, v107, v9, v5
	v_cndmask_b32_e64 v27, v27, v23, s[66:67]
	v_pk_fma_f16 v6, v2, v150, v151 op_sel:[0,0,0] op_sel_hi:[1,0,0] neg_lo:[1,0,0] neg_hi:[1,0,0]
	v_pk_fma_f16 v7, v3, v150, v151 op_sel:[0,0,0] op_sel_hi:[1,0,0] neg_lo:[1,0,0] neg_hi:[1,0,0]
	v_pk_fma_f16 v8, v4, v150, v151 op_sel:[0,0,0] op_sel_hi:[1,0,0] neg_lo:[1,0,0] neg_hi:[1,0,0]
	v_pk_fma_f16 v9, v5, v150, v151 op_sel:[0,0,0] op_sel_hi:[1,0,0] neg_lo:[1,0,0] neg_hi:[1,0,0]
	v_mfma_f32_16x16x32_f16 v[22:25], v[10:13], v[2:5], 0
	ds_read2_b64 v[72:75], v32 offset0:22 offset1:224
	v_pk_fma_f16 v2, v108, v6, v2
	v_pk_fma_f16 v3, v109, v7, v3
	v_pk_fma_f16 v4, v110, v8, v4
	v_pk_fma_f16 v5, v111, v9, v5
	v_cndmask_b32_e64 v28, v28, v20, s[66:67]
.Lc0_next0:
	s_waitcnt lgkmcnt(4)
	v_pk_fma_f16 v6, v2, v120, v121 op_sel:[0,0,0] op_sel_hi:[1,0,0] neg_lo:[1,0,0] neg_hi:[1,0,0]
	v_pk_fma_f16 v7, v3, v120, v121 op_sel:[0,0,0] op_sel_hi:[1,0,0] neg_lo:[1,0,0] neg_hi:[1,0,0]
	v_pk_fma_f16 v8, v4, v120, v121 op_sel:[0,0,0] op_sel_hi:[1,0,0] neg_lo:[1,0,0] neg_hi:[1,0,0]
	v_pk_fma_f16 v9, v5, v120, v121 op_sel:[0,0,0] op_sel_hi:[1,0,0] neg_lo:[1,0,0] neg_hi:[1,0,0]
	v_mfma_f32_16x16x32_f16 v[18:21], v[14:17], v[2:5], 0
	ds_read2_b64 v[76:79], v32 offset0:23 offset1:225
	ds_read_b128 v[132:135], v33 offset:176
	ds_read_b32 v37, v36 offset:8
	ds_read_b32 v38, v36 offset:72
	v_pk_fma_f16 v2, v48, v6, v2
	v_pk_fma_f16 v3, v49, v7, v3
	v_pk_fma_f16 v4, v50, v8, v4
	v_pk_fma_f16 v5, v51, v9, v5
	v_cndmask_b32_e64 v29, v29, v25, s[66:67]
	v_cvt_pk_f16_f32 v30, v26, v27
	v_cvt_pk_f16_f32 v31, v28, v29
	ds_write_b16 v39, v30 offset:2048
	ds_write_b16_d16_hi v39, v30 offset:2112
	ds_write_b16 v39, v31 offset:2176
	ds_write_b16_d16_hi v39, v31 offset:2240
	s_mov_b64 exec, 1
	ds_add_u32 v36, v44 offset:128
	s_mov_b64 exec, -1
	v_pk_fma_f16 v6, v2, v122, v123 op_sel:[0,0,0] op_sel_hi:[1,0,0] neg_lo:[1,0,0] neg_hi:[1,0,0]
	v_pk_fma_f16 v7, v3, v122, v123 op_sel:[0,0,0] op_sel_hi:[1,0,0] neg_lo:[1,0,0] neg_hi:[1,0,0]
	v_pk_fma_f16 v8, v4, v122, v123 op_sel:[0,0,0] op_sel_hi:[1,0,0] neg_lo:[1,0,0] neg_hi:[1,0,0]
	v_pk_fma_f16 v9, v5, v122, v123 op_sel:[0,0,0] op_sel_hi:[1,0,0] neg_lo:[1,0,0] neg_hi:[1,0,0]
	v_mfma_f32_16x16x32_f16 v[22:25], v[14:17], v[2:5], 0
	ds_read2_b64 v[80:83], v32 offset0:24 offset1:226
	v_pk_fma_f16 v2, v52, v6, v2
	v_pk_fma_f16 v3, v53, v7, v3
	v_pk_fma_f16 v4, v54, v8, v4
	v_pk_fma_f16 v5, v55, v9, v5
	v_cndmask_b32_e64 v26, v26, v18, s[60:61]
	v_pk_fma_f16 v6, v2, v124, v125 op_sel:[0,0,0] op_sel_hi:[1,0,0] neg_lo:[1,0,0] neg_hi:[1,0,0]
	v_pk_fma_f16 v7, v3, v124, v125 op_sel:[0,0,0] op_sel_hi:[1,0,0] neg_lo:[1,0,0] neg_hi:[1,0,0]
	v_pk_fma_f16 v8, v4, v124, v125 op_sel:[0,0,0] op_sel_hi:[1,0,0] neg_lo:[1,0,0] neg_hi:[1,0,0]
	v_pk_fma_f16 v9, v5, v124, v125 op_sel:[0,0,0] op_sel_hi:[1,0,0] neg_lo:[1,0,0] neg_hi:[1,0,0]
	v_mfma_f32_16x16x32_f16 v[18:21], v[14:17], v[2:5], 0
	ds_read2_b64 v[84:87], v32 offset0:25 offset1:227
	ds_read_b128 v[136:139], v33 offset:192
	v_pk_fma_f16 v2, v56, v6, v2
	v_pk_fma_f16 v3, v57, v7, v3
	v_pk_fma_f16 v4, v58, v8, v4
	v_pk_fma_f16 v5, v59, v9, v5
	v_cndmask_b32_e64 v27, v27, v23, s[60:61]
	v_pk_fma_f16 v6, v2, v126, v127 op_sel:[0,0,0] op_sel_hi:[1,0,0] neg_lo:[1,0,0] neg_hi:[1,0,0]
	v_pk_fma_f16 v7, v3, v126, v127 op_sel:[0,0,0] op_sel_hi:[1,0,0] neg_lo:[1,0,0] neg_hi:[1,0,0]
	v_pk_fma_f16 v8, v4, v126, v127 op_sel:[0,0,0] op_sel_hi:[1,0,0] neg_lo:[1,0,0] neg_hi:[1,0,0]
	v_pk_fma_f16 v9, v5, v126, v127 op_sel:[0,0,0] op_sel_hi:[1,0,0] neg_lo:[1,0,0] neg_hi:[1,0,0]
	v_mfma_f32_16x16x32_f16 v[22:25], v[14:17], v[2:5], 0
	ds_read2_b64 v[88:91], v32 offset0:26 offset1:228
	v_pk_fma_f16 v2, v60, v6, v2
	v_pk_fma_f16 v3, v61, v7, v3
	v_pk_fma_f16 v4, v62, v8, v4
	v_pk_fma_f16 v5, v63, v9, v5
	v_cndmask_b32_e64 v28, v28, v20, s[60:61]
	s_waitcnt lgkmcnt(11)
	v_pk_fma_f16 v6, v2, v128, v129 op_sel:[0,0,0] op_sel_hi:[1,0,0] neg_lo:[1,0,0] neg_hi:[1,0,0]
	v_pk_fma_f16 v7, v3, v128, v129 op_sel:[0,0,0] op_sel_hi:[1,0,0] neg_lo:[1,0,0] neg_hi:[1,0,0]
	v_pk_fma_f16 v8, v4, v128, v129 op_sel:[0,0,0] op_sel_hi:[1,0,0] neg_lo:[1,0,0] neg_hi:[1,0,0]
	v_pk_fma_f16 v9, v5, v128, v129 op_sel:[0,0,0] op_sel_hi:[1,0,0] neg_lo:[1,0,0] neg_hi:[1,0,0]
	v_mfma_f32_16x16x32_f16 v[18:21], v[14:17], v[2:5], 0
	ds_read2_b64 v[92:95], v32 offset0:27 offset1:229
	ds_read_b128 v[140:143], v33 offset:208
	v_pk_fma_f16 v2, v64, v6, v2
	v_pk_fma_f16 v3, v65, v7, v3
	v_pk_fma_f16 v4, v66, v8, v4
	v_pk_fma_f16 v5, v67, v9, v5
	v_cndmask_b32_e64 v29, v29, v25, s[60:61]
	v_pk_fma_f16 v6, v2, v130, v131 op_sel:[0,0,0] op_sel_hi:[1,0,0] neg_lo:[1,0,0] neg_hi:[1,0,0]
	v_pk_fma_f16 v7, v3, v130, v131 op_sel:[0,0,0] op_sel_hi:[1,0,0] neg_lo:[1,0,0] neg_hi:[1,0,0]
	v_pk_fma_f16 v8, v4, v130, v131 op_sel:[0,0,0] op_sel_hi:[1,0,0] neg_lo:[1,0,0] neg_hi:[1,0,0]
	v_pk_fma_f16 v9, v5, v130, v131 op_sel:[0,0,0] op_sel_hi:[1,0,0] neg_lo:[1,0,0] neg_hi:[1,0,0]
	v_mfma_f32_16x16x32_f16 v[22:25], v[14:17], v[2:5], 0
	ds_read2_b64 v[96:99], v32 offset0:28 offset1:230
	v_pk_fma_f16 v2, v68, v6, v2
	v_pk_fma_f16 v3, v69, v7, v3
	v_pk_fma_f16 v4, v70, v8, v4
	v_pk_fma_f16 v5, v71, v9, v5
	v_cndmask_b32_e64 v26, v26, v18, s[62:63]
	v_pk_fma_f16 v6, v2, v132, v133 op_sel:[0,0,0] op_sel_hi:[1,0,0] neg_lo:[1,0,0] neg_hi:[1,0,0]
	v_pk_fma_f16 v7, v3, v132, v133 op_sel:[0,0,0] op_sel_hi:[1,0,0] neg_lo:[1,0,0] neg_hi:[1,0,0]
	v_pk_fma_f16 v8, v4, v132, v133 op_sel:[0,0,0] op_sel_hi:[1,0,0] neg_lo:[1,0,0] neg_hi:[1,0,0]
	v_pk_fma_f16 v9, v5, v132, v133 op_sel:[0,0,0] op_sel_hi:[1,0,0] neg_lo:[1,0,0] neg_hi:[1,0,0]
	v_mfma_f32_16x16x32_f16 v[18:21], v[14:17], v[2:5], 0
	ds_read2_b64 v[100:103], v32 offset0:29 offset1:231
	ds_read_b128 v[144:147], v33 offset:224
	v_pk_fma_f16 v2, v72, v6, v2
	v_pk_fma_f16 v3, v73, v7, v3
	v_pk_fma_f16 v4, v74, v8, v4
	v_pk_fma_f16 v5, v75, v9, v5
	v_cndmask_b32_e64 v27, v27, v23, s[62:63]
	v_pk_fma_f16 v6, v2, v134, v135 op_sel:[0,0,0] op_sel_hi:[1,0,0] neg_lo:[1,0,0] neg_hi:[1,0,0]
	v_pk_fma_f16 v7, v3, v134, v135 op_sel:[0,0,0] op_sel_hi:[1,0,0] neg_lo:[1,0,0] neg_hi:[1,0,0]
	v_pk_fma_f16 v8, v4, v134, v135 op_sel:[0,0,0] op_sel_hi:[1,0,0] neg_lo:[1,0,0] neg_hi:[1,0,0]
	v_pk_fma_f16 v9, v5, v134, v135 op_sel:[0,0,0] op_sel_hi:[1,0,0] neg_lo:[1,0,0] neg_hi:[1,0,0]
	v_mfma_f32_16x16x32_f16 v[22:25], v[14:17], v[2:5], 0
	ds_read2_b64 v[104:107], v32 offset0:30 offset1:232
	v_pk_fma_f16 v2, v76, v6, v2
	v_pk_fma_f16 v3, v77, v7, v3
	v_pk_fma_f16 v4, v78, v8, v4
	v_pk_fma_f16 v5, v79, v9, v5
	v_cndmask_b32_e64 v28, v28, v20, s[62:63]
	s_waitcnt lgkmcnt(4)
	v_pk_fma_f16 v6, v2, v136, v137 op_sel:[0,0,0] op_sel_hi:[1,0,0] neg_lo:[1,0,0] neg_hi:[1,0,0]
	v_pk_fma_f16 v7, v3, v136, v137 op_sel:[0,0,0] op_sel_hi:[1,0,0] neg_lo:[1,0,0] neg_hi:[1,0,0]
	v_pk_fma_f16 v8, v4, v136, v137 op_sel:[0,0,0] op_sel_hi:[1,0,0] neg_lo:[1,0,0] neg_hi:[1,0,0]
	v_pk_fma_f16 v9, v5, v136, v137 op_sel:[0,0,0] op_sel_hi:[1,0,0] neg_lo:[1,0,0] neg_hi:[1,0,0]
	v_mfma_f32_16x16x32_f16 v[18:21], v[14:17], v[2:5], 0
	ds_read2_b64 v[108:111], v32 offset0:31 offset1:233
	ds_read_b128 v[148:151], v33 offset:240
	v_pk_fma_f16 v2, v80, v6, v2
	v_pk_fma_f16 v3, v81, v7, v3
	v_pk_fma_f16 v4, v82, v8, v4
	v_pk_fma_f16 v5, v83, v9, v5
	v_cndmask_b32_e64 v29, v29, v25, s[62:63]
	v_readfirstlane_b32 s4, v37
	v_readfirstlane_b32 s5, v38
	s_and_b32 s4, s4, s5
	s_cbranch_scc0 .Lc0_slow1
.Lc0_back1:
	v_pk_fma_f16 v6, v2, v138, v139 op_sel:[0,0,0] op_sel_hi:[1,0,0] neg_lo:[1,0,0] neg_hi:[1,0,0]
	v_pk_fma_f16 v7, v3, v138, v139 op_sel:[0,0,0] op_sel_hi:[1,0,0] neg_lo:[1,0,0] neg_hi:[1,0,0]
	v_pk_fma_f16 v8, v4, v138, v139 op_sel:[0,0,0] op_sel_hi:[1,0,0] neg_lo:[1,0,0] neg_hi:[1,0,0]
	v_pk_fma_f16 v9, v5, v138, v139 op_sel:[0,0,0] op_sel_hi:[1,0,0] neg_lo:[1,0,0] neg_hi:[1,0,0]
	v_mfma_f32_16x16x32_f16 v[22:25], v[14:17], v[2:5], 0
	ds_read2_b64 v[48:51], v32 offset0:32 offset1:234
	v_pk_fma_f16 v2, v84, v6, v2
	v_pk_fma_f16 v3, v85, v7, v3
	v_pk_fma_f16 v4, v86, v8, v4
	v_pk_fma_f16 v5, v87, v9, v5
	v_cndmask_b32_e64 v26, v26, v18, s[64:65]
	v_pk_fma_f16 v6, v2, v140, v141 op_sel:[0,0,0] op_sel_hi:[1,0,0] neg_lo:[1,0,0] neg_hi:[1,0,0]
	v_pk_fma_f16 v7, v3, v140, v141 op_sel:[0,0,0] op_sel_hi:[1,0,0] neg_lo:[1,0,0] neg_hi:[1,0,0]
	v_pk_fma_f16 v8, v4, v140, v141 op_sel:[0,0,0] op_sel_hi:[1,0,0] neg_lo:[1,0,0] neg_hi:[1,0,0]
	v_pk_fma_f16 v9, v5, v140, v141 op_sel:[0,0,0] op_sel_hi:[1,0,0] neg_lo:[1,0,0] neg_hi:[1,0,0]
	v_mfma_f32_16x16x32_f16 v[18:21], v[14:17], v[2:5], 0
	ds_read2_b64 v[52:55], v32 offset0:33 offset1:235
	ds_read_b128 v[120:123], v33 offset:256
	ds_read2_b64 v[10:13], v34 offset0:32 offset1:234
	v_pk_fma_f16 v2, v88, v6, v2
	v_pk_fma_f16 v3, v89, v7, v3
	v_pk_fma_f16 v4, v90, v8, v4
	v_pk_fma_f16 v5, v91, v9, v5
	v_cndmask_b32_e64 v27, v27, v23, s[64:65]
	v_pk_fma_f16 v6, v2, v142, v143 op_sel:[0,0,0] op_sel_hi:[1,0,0] neg_lo:[1,0,0] neg_hi:[1,0,0]
	v_pk_fma_f16 v7, v3, v142, v143 op_sel:[0,0,0] op_sel_hi:[1,0,0] neg_lo:[1,0,0] neg_hi:[1,0,0]
	v_pk_fma_f16 v8, v4, v142, v143 op_sel:[0,0,0] op_sel_hi:[1,0,0] neg_lo:[1,0,0] neg_hi:[1,0,0]
	v_pk_fma_f16 v9, v5, v142, v143 op_sel:[0,0,0] op_sel_hi:[1,0,0] neg_lo:[1,0,0] neg_hi:[1,0,0]
	v_mfma_f32_16x16x32_f16 v[22:25], v[14:17], v[2:5], 0
	ds_read2_b64 v[56:59], v32 offset0:34 offset1:236
	v_pk_fma_f16 v2, v92, v6, v2
	v_pk_fma_f16 v3, v93, v7, v3
	v_pk_fma_f16 v4, v94, v8, v4
	v_pk_fma_f16 v5, v95, v9, v5
	v_cndmask_b32_e64 v28, v28, v20, s[64:65]
	s_waitcnt lgkmcnt(5)
	v_pk_fma_f16 v6, v2, v144, v145 op_sel:[0,0,0] op_sel_hi:[1,0,0] neg_lo:[1,0,0] neg_hi:[1,0,0]
	v_pk_fma_f16 v7, v3, v144, v145 op_sel:[0,0,0] op_sel_hi:[1,0,0] neg_lo:[1,0,0] neg_hi:[1,0,0]
	v_pk_fma_f16 v8, v4, v144, v145 op_sel:[0,0,0] op_sel_hi:[1,0,0] neg_lo:[1,0,0] neg_hi:[1,0,0]
	v_pk_fma_f16 v9, v5, v144, v145 op_sel:[0,0,0] op_sel_hi:[1,0,0] neg_lo:[1,0,0] neg_hi:[1,0,0]
	v_mfma_f32_16x16x32_f16 v[18:21], v[14:17], v[2:5], 0
	ds_read2_b64 v[60:63], v32 offset0:35 offset1:237
	ds_read_b128 v[124:127], v33 offset:272
	v_pk_fma_f16 v2, v96, v6, v2
	v_pk_fma_f16 v3, v97, v7, v3
	v_pk_fma_f16 v4, v98, v8, v4
	v_pk_fma_f16 v5, v99, v9, v5
	v_cndmask_b32_e64 v29, v29, v25, s[64:65]
	v_pk_fma_f16 v6, v2, v146, v147 op_sel:[0,0,0] op_sel_hi:[1,0,0] neg_lo:[1,0,0] neg_hi:[1,0,0]
	v_pk_fma_f16 v7, v3, v146, v147 op_sel:[0,0,0] op_sel_hi:[1,0,0] neg_lo:[1,0,0] neg_hi:[1,0,0]
	v_pk_fma_f16 v8, v4, v146, v147 op_sel:[0,0,0] op_sel_hi:[1,0,0] neg_lo:[1,0,0] neg_hi:[1,0,0]
	v_pk_fma_f16 v9, v5, v146, v147 op_sel:[0,0,0] op_sel_hi:[1,0,0] neg_lo:[1,0,0] neg_hi:[1,0,0]
	v_mfma_f32_16x16x32_f16 v[22:25], v[14:17], v[2:5], 0
	ds_read2_b64 v[64:67], v32 offset0:36 offset1:238
	v_pk_fma_f16 v2, v100, v6, v2
	v_pk_fma_f16 v3, v101, v7, v3
	v_pk_fma_f16 v4, v102, v8, v4
	v_pk_fma_f16 v5, v103, v9, v5
	v_cndmask_b32_e64 v26, v26, v18, s[66:67]
	v_pk_fma_f16 v6, v2, v148, v149 op_sel:[0,0,0] op_sel_hi:[1,0,0] neg_lo:[1,0,0] neg_hi:[1,0,0]
	v_pk_fma_f16 v7, v3, v148, v149 op_sel:[0,0,0] op_sel_hi:[1,0,0] neg_lo:[1,0,0] neg_hi:[1,0,0]
	v_pk_fma_f16 v8, v4, v148, v149 op_sel:[0,0,0] op_sel_hi:[1,0,0] neg_lo:[1,0,0] neg_hi:[1,0,0]
	v_pk_fma_f16 v9, v5, v148, v149 op_sel:[0,0,0] op_sel_hi:[1,0,0] neg_lo:[1,0,0] neg_hi:[1,0,0]
	v_mfma_f32_16x16x32_f16 v[18:21], v[14:17], v[2:5], 0
	ds_read2_b64 v[68:71], v32 offset0:37 offset1:239
	ds_read_b128 v[128:131], v33 offset:288
	v_pk_fma_f16 v2, v104, v6, v2
	v_pk_fma_f16 v3, v105, v7, v3
	v_pk_fma_f16 v4, v106, v8, v4
	v_pk_fma_f16 v5, v107, v9, v5
	v_cndmask_b32_e64 v27, v27, v23, s[66:67]
	v_pk_fma_f16 v6, v2, v150, v151 op_sel:[0,0,0] op_sel_hi:[1,0,0] neg_lo:[1,0,0] neg_hi:[1,0,0]
	v_pk_fma_f16 v7, v3, v150, v151 op_sel:[0,0,0] op_sel_hi:[1,0,0] neg_lo:[1,0,0] neg_hi:[1,0,0]
	v_pk_fma_f16 v8, v4, v150, v151 op_sel:[0,0,0] op_sel_hi:[1,0,0] neg_lo:[1,0,0] neg_hi:[1,0,0]
	v_pk_fma_f16 v9, v5, v150, v151 op_sel:[0,0,0] op_sel_hi:[1,0,0] neg_lo:[1,0,0] neg_hi:[1,0,0]
	v_mfma_f32_16x16x32_f16 v[22:25], v[14:17], v[2:5], 0
	ds_read2_b64 v[72:75], v32 offset0:38 offset1:240
	v_pk_fma_f16 v2, v108, v6, v2
	v_pk_fma_f16 v3, v109, v7, v3
	v_pk_fma_f16 v4, v110, v8, v4
	v_pk_fma_f16 v5, v111, v9, v5
	v_cndmask_b32_e64 v28, v28, v20, s[66:67]
.Lc0_next1:
	v_add_u32_e32 v32, 0x100, v32
	v_add_u32_e32 v33, 0x100, v33
	v_add_u32_e32 v34, 0x100, v34
	v_add_u32_e32 v36, 8, v36
	v_add_u32_e32 v39, 0x1000, v39
	v_add_u32_e32 v43, 0x1000, v43
	v_add_u32_e32 v35, 0x800, v35
	s_xor_b32 s71, s71, 2
	s_add_i32 s70, s70, 1
	s_cmp_lt_u32 s70, 6
	s_cbranch_scc1 .Lc0_loop
	s_waitcnt lgkmcnt(4)
	v_pk_fma_f16 v6, v2, v120, v121 op_sel:[0,0,0] op_sel_hi:[1,0,0] neg_lo:[1,0,0] neg_hi:[1,0,0]
	v_pk_fma_f16 v7, v3, v120, v121 op_sel:[0,0,0] op_sel_hi:[1,0,0] neg_lo:[1,0,0] neg_hi:[1,0,0]
	v_pk_fma_f16 v8, v4, v120, v121 op_sel:[0,0,0] op_sel_hi:[1,0,0] neg_lo:[1,0,0] neg_hi:[1,0,0]
	v_pk_fma_f16 v9, v5, v120, v121 op_sel:[0,0,0] op_sel_hi:[1,0,0] neg_lo:[1,0,0] neg_hi:[1,0,0]
	v_mfma_f32_16x16x32_f16 v[18:21], v[10:13], v[2:5], 0
	ds_read2_b64 v[76:79], v32 offset0:7 offset1:209
	ds_read_b128 v[132:135], v33 offset:48
	v_pk_fma_f16 v2, v48, v6, v2
	v_pk_fma_f16 v3, v49, v7, v3
	v_pk_fma_f16 v4, v50, v8, v4
	v_pk_fma_f16 v5, v51, v9, v5
	v_cndmask_b32_e64 v29, v29, v25, s[66:67]
	v_cvt_pk_f16_f32 v30, v26, v27
	v_cvt_pk_f16_f32 v31, v28, v29
	ds_write_b16 v39, v30 offset:0
	ds_write_b16_d16_hi v39, v30 offset:64
	ds_write_b16 v39, v31 offset:128
	ds_write_b16_d16_hi v39, v31 offset:192
	s_mov_b64 exec, 1
	ds_add_u32 v36, v44 offset:124
	s_mov_b64 exec, -1
	v_pk_fma_f16 v6, v2, v122, v123 op_sel:[0,0,0] op_sel_hi:[1,0,0] neg_lo:[1,0,0] neg_hi:[1,0,0]
	v_pk_fma_f16 v7, v3, v122, v123 op_sel:[0,0,0] op_sel_hi:[1,0,0] neg_lo:[1,0,0] neg_hi:[1,0,0]
	v_pk_fma_f16 v8, v4, v122, v123 op_sel:[0,0,0] op_sel_hi:[1,0,0] neg_lo:[1,0,0] neg_hi:[1,0,0]
	v_pk_fma_f16 v9, v5, v122, v123 op_sel:[0,0,0] op_sel_hi:[1,0,0] neg_lo:[1,0,0] neg_hi:[1,0,0]
	v_mfma_f32_16x16x32_f16 v[22:25], v[10:13], v[2:5], 0
	v_pk_fma_f16 v2, v52, v6, v2
	v_pk_fma_f16 v3, v53, v7, v3
	v_pk_fma_f16 v4, v54, v8, v4
	v_pk_fma_f16 v5, v55, v9, v5
	v_cndmask_b32_e64 v26, v26, v18, s[60:61]
	v_pk_fma_f16 v6, v2, v124, v125 op_sel:[0,0,0] op_sel_hi:[1,0,0] neg_lo:[1,0,0] neg_hi:[1,0,0]
	v_pk_fma_f16 v7, v3, v124, v125 op_sel:[0,0,0] op_sel_hi:[1,0,0] neg_lo:[1,0,0] neg_hi:[1,0,0]
	v_pk_fma_f16 v8, v4, v124, v125 op_sel:[0,0,0] op_sel_hi:[1,0,0] neg_lo:[1,0,0] neg_hi:[1,0,0]
	v_pk_fma_f16 v9, v5, v124, v125 op_sel:[0,0,0] op_sel_hi:[1,0,0] neg_lo:[1,0,0] neg_hi:[1,0,0]
	v_mfma_f32_16x16x32_f16 v[18:21], v[10:13], v[2:5], 0
	v_pk_fma_f16 v2, v56, v6, v2
	v_pk_fma_f16 v3, v57, v7, v3
	v_pk_fma_f16 v4, v58, v8, v4
	v_pk_fma_f16 v5, v59, v9, v5
	v_cndmask_b32_e64 v27, v27, v23, s[60:61]
	v_pk_fma_f16 v6, v2, v126, v127 op_sel:[0,0,0] op_sel_hi:[1,0,0] neg_lo:[1,0,0] neg_hi:[1,0,0]
	v_pk_fma_f16 v7, v3, v126, v127 op_sel:[0,0,0] op_sel_hi:[1,0,0] neg_lo:[1,0,0] neg_hi:[1,0,0]
	v_pk_fma_f16 v8, v4, v126, v127 op_sel:[0,0,0] op_sel_hi:[1,0,0] neg_lo:[1,0,0] neg_hi:[1,0,0]
	v_pk_fma_f16 v9, v5, v126, v127 op_sel:[0,0,0] op_sel_hi:[1,0,0] neg_lo:[1,0,0] neg_hi:[1,0,0]
	v_mfma_f32_16x16x32_f16 v[22:25], v[10:13], v[2:5], 0
	v_pk_fma_f16 v2, v60, v6, v2
	v_pk_fma_f16 v3, v61, v7, v3
	v_pk_fma_f16 v4, v62, v8, v4
	v_pk_fma_f16 v5, v63, v9, v5
	v_cndmask_b32_e64 v28, v28, v20, s[60:61]
	s_waitcnt lgkmcnt(5)
	v_pk_fma_f16 v6, v2, v128, v129 op_sel:[0,0,0] op_sel_hi:[1,0,0] neg_lo:[1,0,0] neg_hi:[1,0,0]
	v_pk_fma_f16 v7, v3, v128, v129 op_sel:[0,0,0] op_sel_hi:[1,0,0] neg_lo:[1,0,0] neg_hi:[1,0,0]
	v_pk_fma_f16 v8, v4, v128, v129 op_sel:[0,0,0] op_sel_hi:[1,0,0] neg_lo:[1,0,0] neg_hi:[1,0,0]
	v_pk_fma_f16 v9, v5, v128, v129 op_sel:[0,0,0] op_sel_hi:[1,0,0] neg_lo:[1,0,0] neg_hi:[1,0,0]
	v_mfma_f32_16x16x32_f16 v[18:21], v[10:13], v[2:5], 0
	v_pk_fma_f16 v2, v64, v6, v2
	v_pk_fma_f16 v3, v65, v7, v3
	v_pk_fma_f16 v4, v66, v8, v4
	v_pk_fma_f16 v5, v67, v9, v5
	v_cndmask_b32_e64 v29, v29, v25, s[60:61]
	v_pk_fma_f16 v6, v2, v130, v131 op_sel:[0,0,0] op_sel_hi:[1,0,0] neg_lo:[1,0,0] neg_hi:[1,0,0]
	v_pk_fma_f16 v7, v3, v130, v131 op_sel:[0,0,0] op_sel_hi:[1,0,0] neg_lo:[1,0,0] neg_hi:[1,0,0]
	v_pk_fma_f16 v8, v4, v130, v131 op_sel:[0,0,0] op_sel_hi:[1,0,0] neg_lo:[1,0,0] neg_hi:[1,0,0]
	v_pk_fma_f16 v9, v5, v130, v131 op_sel:[0,0,0] op_sel_hi:[1,0,0] neg_lo:[1,0,0] neg_hi:[1,0,0]
	v_mfma_f32_16x16x32_f16 v[22:25], v[10:13], v[2:5], 0
	v_pk_fma_f16 v2, v68, v6, v2
	v_pk_fma_f16 v3, v69, v7, v3
	v_pk_fma_f16 v4, v70, v8, v4
	v_pk_fma_f16 v5, v71, v9, v5
	v_cndmask_b32_e64 v26, v26, v18, s[62:63]
	v_pk_fma_f16 v6, v2, v132, v133 op_sel:[0,0,0] op_sel_hi:[1,0,0] neg_lo:[1,0,0] neg_hi:[1,0,0]
	v_pk_fma_f16 v7, v3, v132, v133 op_sel:[0,0,0] op_sel_hi:[1,0,0] neg_lo:[1,0,0] neg_hi:[1,0,0]
	v_pk_fma_f16 v8, v4, v132, v133 op_sel:[0,0,0] op_sel_hi:[1,0,0] neg_lo:[1,0,0] neg_hi:[1,0,0]
	v_pk_fma_f16 v9, v5, v132, v133 op_sel:[0,0,0] op_sel_hi:[1,0,0] neg_lo:[1,0,0] neg_hi:[1,0,0]
	v_mfma_f32_16x16x32_f16 v[18:21], v[10:13], v[2:5], 0
	v_pk_fma_f16 v2, v72, v6, v2
	v_pk_fma_f16 v3, v73, v7, v3
	v_pk_fma_f16 v4, v74, v8, v4
	v_pk_fma_f16 v5, v75, v9, v5
	v_cndmask_b32_e64 v27, v27, v23, s[62:63]
	v_pk_fma_f16 v6, v2, v134, v135 op_sel:[0,0,0] op_sel_hi:[1,0,0] neg_lo:[1,0,0] neg_hi:[1,0,0]
	v_pk_fma_f16 v7, v3, v134, v135 op_sel:[0,0,0] op_sel_hi:[1,0,0] neg_lo:[1,0,0] neg_hi:[1,0,0]
	v_pk_fma_f16 v8, v4, v134, v135 op_sel:[0,0,0] op_sel_hi:[1,0,0] neg_lo:[1,0,0] neg_hi:[1,0,0]
	v_pk_fma_f16 v9, v5, v134, v135 op_sel:[0,0,0] op_sel_hi:[1,0,0] neg_lo:[1,0,0] neg_hi:[1,0,0]
	v_mfma_f32_16x16x32_f16 v[22:25], v[10:13], v[2:5], 0
	v_pk_fma_f16 v2, v76, v6, v2
	v_pk_fma_f16 v3, v77, v7, v3
	v_pk_fma_f16 v4, v78, v8, v4
	v_pk_fma_f16 v5, v79, v9, v5
	v_cndmask_b32_e64 v28, v28, v20, s[62:63]
	s_nop 7
	v_cndmask_b32_e64 v29, v29, v25, s[62:63]
	v_cvt_pk_f16_f32 v30, v26, v27
	v_cvt_pk_f16_f32 v31, v28, v29
	ds_write_b16 v39, v30 offset:2048
	ds_write_b16_d16_hi v39, v30 offset:2112
	ds_write_b16 v39, v31 offset:2176
	ds_write_b16_d16_hi v39, v31 offset:2240
	s_mov_b64 exec, 1
	ds_add_u32 v36, v44 offset:128
	s_mov_b64 exec, -1
	s_branch .Lc0_end

.Lc_par1:
	ds_read2_b64 v[48:51], v32 offset0:0 offset1:202
	ds_read2_b64 v[52:55], v32 offset0:1 offset1:203
	ds_read_b128 v[120:123], v33 offset:0
	ds_read2_b64 v[10:13], v34 offset0:0 offset1:202
	ds_read2_b64 v[56:59], v32 offset0:2 offset1:204
	ds_read2_b64 v[60:63], v32 offset0:3 offset1:205
	ds_read_b128 v[124:127], v33 offset:16
	ds_read2_b64 v[64:67], v32 offset0:4 offset1:206
	ds_read2_b64 v[68:71], v32 offset0:5 offset1:207
	ds_read_b128 v[128:131], v33 offset:32
	ds_read2_b64 v[72:75], v32 offset0:6 offset1:208
	s_mov_b32 s70, 0
	s_mov_b32 s71, 0
.Lc1_loop:
	s_waitcnt lgkmcnt(4)
	v_pk_fma_f16 v6, v2, v120, v121 op_sel:[0,1,1] op_sel_hi:[1,1,1] neg_lo:[1,0,0] neg_hi:[1,0,0]
	v_pk_fma_f16 v7, v3, v120, v121 op_sel:[0,1,1] op_sel_hi:[1,1,1] neg_lo:[1,0,0] neg_hi:[1,0,0]
	v_pk_fma_f16 v8, v4, v120, v121 op_sel:[0,1,1] op_sel_hi:[1,1,1] neg_lo:[1,0,0] neg_hi:[1,0,0]
	v_pk_fma_f16 v9, v5, v120, v121 op_sel:[0,1,1] op_sel_hi:[1,1,1] neg_lo:[1,0,0] neg_hi:[1,0,0]
	v_mfma_f32_16x16x32_f16 v[18:21], v[10:13], v[2:5], 0
	ds_read2_b64 v[76:79], v32 offset0:7 offset1:209
	ds_read_b128 v[132:135], v33 offset:48
	ds_read_b32 v37, v36 offset:4
	ds_read_b32 v38, v36 offset:68
	v_pk_fma_f16 v2, v48, v6, v2
	v_pk_fma_f16 v3, v49, v7, v3
	v_pk_fma_f16 v4, v50, v8, v4
	v_pk_fma_f16 v5, v51, v9, v5
	v_cndmask_b32_e64 v29, v29, v25, s[66:67]
	v_cvt_pk_f16_f32 v30, v26, v27
	v_cvt_pk_f16_f32 v31, v28, v29
	ds_write_b16 v39, v30 offset:0
	ds_write_b16_d16_hi v39, v30 offset:64
	ds_write_b16 v39, v31 offset:128
	ds_write_b16_d16_hi v39, v31 offset:192
	s_mov_b64 exec, 1
	ds_add_u32 v36, v44 offset:124
	s_mov_b64 exec, -1
	v_pk_fma_f16 v6, v2, v122, v123 op_sel:[0,1,1] op_sel_hi:[1,1,1] neg_lo:[1,0,0] neg_hi:[1,0,0]
	v_pk_fma_f16 v7, v3, v122, v123 op_sel:[0,1,1] op_sel_hi:[1,1,1] neg_lo:[1,0,0] neg_hi:[1,0,0]
	v_pk_fma_f16 v8, v4, v122, v123 op_sel:[0,1,1] op_sel_hi:[1,1,1] neg_lo:[1,0,0] neg_hi:[1,0,0]
	v_pk_fma_f16 v9, v5, v122, v123 op_sel:[0,1,1] op_sel_hi:[1,1,1] neg_lo:[1,0,0] neg_hi:[1,0,0]
	v_mfma_f32_16x16x32_f16 v[22:25], v[10:13], v[2:5], 0
	ds_read2_b64 v[80:83], v32 offset0:8 offset1:210
	v_pk_fma_f16 v2, v52, v6, v2
	v_pk_fma_f16 v3, v53, v7, v3
	v_pk_fma_f16 v4, v54, v8, v4
	v_pk_fma_f16 v5, v55, v9, v5
	v_cndmask_b32_e64 v26, v26, v18, s[60:61]
	v_pk_fma_f16 v6, v2, v124, v125 op_sel:[0,1,1] op_sel_hi:[1,1,1] neg_lo:[1,0,0] neg_hi:[1,0,0]
	v_pk_fma_f16 v7, v3, v124, v125 op_sel:[0,1,1] op_sel_hi:[1,1,1] neg_lo:[1,0,0] neg_hi:[1,0,0]
	v_pk_fma_f16 v8, v4, v124, v125 op_sel:[0,1,1] op_sel_hi:[1,1,1] neg_lo:[1,0,0] neg_hi:[1,0,0]
	v_pk_fma_f16 v9, v5, v124, v125 op_sel:[0,1,1] op_sel_hi:[1,1,1] neg_lo:[1,0,0] neg_hi:[1,0,0]
	v_mfma_f32_16x16x32_f16 v[18:21], v[10:13], v[2:5], 0
	ds_read2_b64 v[84:87], v32 offset0:9 offset1:211
	ds_read_b128 v[136:139], v33 offset:64
	v_pk_fma_f16 v2, v56, v6, v2
	v_pk_fma_f16 v3, v57, v7, v3
	v_pk_fma_f16 v4, v58, v8, v4
	v_pk_fma_f16 v5, v59, v9, v5
	v_cndmask_b32_e64 v27, v27, v23, s[60:61]
	v_pk_fma_f16 v6, v2, v126, v127 op_sel:[0,1,1] op_sel_hi:[1,1,1] neg_lo:[1,0,0] neg_hi:[1,0,0]
	v_pk_fma_f16 v7, v3, v126, v127 op_sel:[0,1,1] op_sel_hi:[1,1,1] neg_lo:[1,0,0] neg_hi:[1,0,0]
	v_pk_fma_f16 v8, v4, v126, v127 op_sel:[0,1,1] op_sel_hi:[1,1,1] neg_lo:[1,0,0] neg_hi:[1,0,0]
	v_pk_fma_f16 v9, v5, v126, v127 op_sel:[0,1,1] op_sel_hi:[1,1,1] neg_lo:[1,0,0] neg_hi:[1,0,0]
	v_mfma_f32_16x16x32_f16 v[22:25], v[10:13], v[2:5], 0
	ds_read2_b64 v[88:91], v32 offset0:10 offset1:212
	v_pk_fma_f16 v2, v60, v6, v2
	v_pk_fma_f16 v3, v61, v7, v3
	v_pk_fma_f16 v4, v62, v8, v4
	v_pk_fma_f16 v5, v63, v9, v5
	v_cndmask_b32_e64 v28, v28, v20, s[60:61]
	s_waitcnt lgkmcnt(11)
	v_pk_fma_f16 v6, v2, v128, v129 op_sel:[0,1,1] op_sel_hi:[1,1,1] neg_lo:[1,0,0] neg_hi:[1,0,0]
	v_pk_fma_f16 v7, v3, v128, v129 op_sel:[0,1,1] op_sel_hi:[1,1,1] neg_lo:[1,0,0] neg_hi:[1,0,0]
	v_pk_fma_f16 v8, v4, v128, v129 op_sel:[0,1,1] op_sel_hi:[1,1,1] neg_lo:[1,0,0] neg_hi:[1,0,0]
	v_pk_fma_f16 v9, v5, v128, v129 op_sel:[0,1,1] op_sel_hi:[1,1,1] neg_lo:[1,0,0] neg_hi:[1,0,0]
	v_mfma_f32_16x16x32_f16 v[18:21], v[10:13], v[2:5], 0
	ds_read2_b64 v[92:95], v32 offset0:11 offset1:213
	ds_read_b128 v[140:143], v33 offset:80
	v_pk_fma_f16 v2, v64, v6, v2
	v_pk_fma_f16 v3, v65, v7, v3
	v_pk_fma_f16 v4, v66, v8, v4
	v_pk_fma_f16 v5, v67, v9, v5
	v_cndmask_b32_e64 v29, v29, v25, s[60:61]
	v_pk_fma_f16 v6, v2, v130, v131 op_sel:[0,1,1] op_sel_hi:[1,1,1] neg_lo:[1,0,0] neg_hi:[1,0,0]
	v_pk_fma_f16 v7, v3, v130, v131 op_sel:[0,1,1] op_sel_hi:[1,1,1] neg_lo:[1,0,0] neg_hi:[1,0,0]
	v_pk_fma_f16 v8, v4, v130, v131 op_sel:[0,1,1] op_sel_hi:[1,1,1] neg_lo:[1,0,0] neg_hi:[1,0,0]
	v_pk_fma_f16 v9, v5, v130, v131 op_sel:[0,1,1] op_sel_hi:[1,1,1] neg_lo:[1,0,0] neg_hi:[1,0,0]
	v_mfma_f32_16x16x32_f16 v[22:25], v[10:13], v[2:5], 0
	ds_read2_b64 v[96:99], v32 offset0:12 offset1:214
	v_pk_fma_f16 v2, v68, v6, v2
	v_pk_fma_f16 v3, v69, v7, v3
	v_pk_fma_f16 v4, v70, v8, v4
	v_pk_fma_f16 v5, v71, v9, v5
	v_cndmask_b32_e64 v26, v26, v18, s[62:63]
	v_pk_fma_f16 v6, v2, v132, v133 op_sel:[0,1,1] op_sel_hi:[1,1,1] neg_lo:[1,0,0] neg_hi:[1,0,0]
	v_pk_fma_f16 v7, v3, v132, v133 op_sel:[0,1,1] op_sel_hi:[1,1,1] neg_lo:[1,0,0] neg_hi:[1,0,0]
	v_pk_fma_f16 v8, v4, v132, v133 op_sel:[0,1,1] op_sel_hi:[1,1,1] neg_lo:[1,0,0] neg_hi:[1,0,0]
	v_pk_fma_f16 v9, v5, v132, v133 op_sel:[0,1,1] op_sel_hi:[1,1,1] neg_lo:[1,0,0] neg_hi:[1,0,0]
	v_mfma_f32_16x16x32_f16 v[18:21], v[10:13], v[2:5], 0
	ds_read2_b64 v[100:103], v32 offset0:13 offset1:215
	ds_read_b128 v[144:147], v33 offset:96
	v_pk_fma_f16 v2, v72, v6, v2
	v_pk_fma_f16 v3, v73, v7, v3
	v_pk_fma_f16 v4, v74, v8, v4
	v_pk_fma_f16 v5, v75, v9, v5
	v_cndmask_b32_e64 v27, v27, v23, s[62:63]
	v_pk_fma_f16 v6, v2, v134, v135 op_sel:[0,1,1] op_sel_hi:[1,1,1] neg_lo:[1,0,0] neg_hi:[1,0,0]
	v_pk_fma_f16 v7, v3, v134, v135 op_sel:[0,1,1] op_sel_hi:[1,1,1] neg_lo:[1,0,0] neg_hi:[1,0,0]
	v_pk_fma_f16 v8, v4, v134, v135 op_sel:[0,1,1] op_sel_hi:[1,1,1] neg_lo:[1,0,0] neg_hi:[1,0,0]
	v_pk_fma_f16 v9, v5, v134, v135 op_sel:[0,1,1] op_sel_hi:[1,1,1] neg_lo:[1,0,0] neg_hi:[1,0,0]
	v_mfma_f32_16x16x32_f16 v[22:25], v[10:13], v[2:5], 0
	ds_read2_b64 v[104:107], v32 offset0:14 offset1:216
	v_pk_fma_f16 v2, v76, v6, v2
	v_pk_fma_f16 v3, v77, v7, v3
	v_pk_fma_f16 v4, v78, v8, v4
	v_pk_fma_f16 v5, v79, v9, v5
	v_cndmask_b32_e64 v28, v28, v20, s[62:63]
	s_waitcnt lgkmcnt(4)
	v_pk_fma_f16 v6, v2, v136, v137 op_sel:[0,1,1] op_sel_hi:[1,1,1] neg_lo:[1,0,0] neg_hi:[1,0,0]
	v_pk_fma_f16 v7, v3, v136, v137 op_sel:[0,1,1] op_sel_hi:[1,1,1] neg_lo:[1,0,0] neg_hi:[1,0,0]
	v_pk_fma_f16 v8, v4, v136, v137 op_sel:[0,1,1] op_sel_hi:[1,1,1] neg_lo:[1,0,0] neg_hi:[1,0,0]
	v_pk_fma_f16 v9, v5, v136, v137 op_sel:[0,1,1] op_sel_hi:[1,1,1] neg_lo:[1,0,0] neg_hi:[1,0,0]
	v_mfma_f32_16x16x32_f16 v[18:21], v[10:13], v[2:5], 0
	ds_read2_b64 v[108:111], v32 offset0:15 offset1:217
	ds_read_b128 v[148:151], v33 offset:112
	v_pk_fma_f16 v2, v80, v6, v2
	v_pk_fma_f16 v3, v81, v7, v3
	v_pk_fma_f16 v4, v82, v8, v4
	v_pk_fma_f16 v5, v83, v9, v5
	v_cndmask_b32_e64 v29, v29, v25, s[62:63]
	v_readfirstlane_b32 s4, v37
	v_readfirstlane_b32 s5, v38
	s_and_b32 s4, s4, s5
	s_cbranch_scc0 .Lc1_slow0

.Lc1_nd0:
	v_pk_fma_f16 v6, v2, v138, v139 op_sel:[0,1,1] op_sel_hi:[1,1,1] neg_lo:[1,0,0] neg_hi:[1,0,0]
	v_pk_fma_f16 v7, v3, v138, v139 op_sel:[0,1,1] op_sel_hi:[1,1,1] neg_lo:[1,0,0] neg_hi:[1,0,0]
	v_pk_fma_f16 v8, v4, v138, v139 op_sel:[0,1,1] op_sel_hi:[1,1,1] neg_lo:[1,0,0] neg_hi:[1,0,0]
	v_pk_fma_f16 v9, v5, v138, v139 op_sel:[0,1,1] op_sel_hi:[1,1,1] neg_lo:[1,0,0] neg_hi:[1,0,0]
	v_mfma_f32_16x16x32_f16 v[22:25], v[10:13], v[2:5], 0
	ds_read2_b64 v[48:51], v32 offset0:16 offset1:218
	v_pk_fma_f16 v2, v84, v6, v2
	v_pk_fma_f16 v3, v85, v7, v3
	v_pk_fma_f16 v4, v86, v8, v4
	v_pk_fma_f16 v5, v87, v9, v5
	v_cndmask_b32_e64 v26, v26, v18, s[64:65]
	v_pk_fma_f16 v6, v2, v140, v141 op_sel:[0,1,1] op_sel_hi:[1,1,1] neg_lo:[1,0,0] neg_hi:[1,0,0]
	v_pk_fma_f16 v7, v3, v140, v141 op_sel:[0,1,1] op_sel_hi:[1,1,1] neg_lo:[1,0,0] neg_hi:[1,0,0]
	v_pk_fma_f16 v8, v4, v140, v141 op_sel:[0,1,1] op_sel_hi:[1,1,1] neg_lo:[1,0,0] neg_hi:[1,0,0]
	v_pk_fma_f16 v9, v5, v140, v141 op_sel:[0,1,1] op_sel_hi:[1,1,1] neg_lo:[1,0,0] neg_hi:[1,0,0]
	v_mfma_f32_16x16x32_f16 v[18:21], v[10:13], v[2:5], 0
	ds_read2_b64 v[52:55], v32 offset0:17 offset1:219
	ds_read_b128 v[120:123], v33 offset:128
	ds_read2_b64 v[14:17], v34 offset0:16 offset1:218
	v_pk_fma_f16 v2, v88, v6, v2
	v_pk_fma_f16 v3, v89, v7, v3
	v_pk_fma_f16 v4, v90, v8, v4
	v_pk_fma_f16 v5, v91, v9, v5
	v_cndmask_b32_e64 v27, v27, v23, s[64:65]
	v_pk_fma_f16 v6, v2, v142, v143 op_sel:[0,1,1] op_sel_hi:[1,1,1] neg_lo:[1,0,0] neg_hi:[1,0,0]
	v_pk_fma_f16 v7, v3, v142, v143 op_sel:[0,1,1] op_sel_hi:[1,1,1] neg_lo:[1,0,0] neg_hi:[1,0,0]
	v_pk_fma_f16 v8, v4, v142, v143 op_sel:[0,1,1] op_sel_hi:[1,1,1] neg_lo:[1,0,0] neg_hi:[1,0,0]
	v_pk_fma_f16 v9, v5, v142, v143 op_sel:[0,1,1] op_sel_hi:[1,1,1] neg_lo:[1,0,0] neg_hi:[1,0,0]
	v_mfma_f32_16x16x32_f16 v[22:25], v[10:13], v[2:5], 0
	ds_read2_b64 v[56:59], v32 offset0:18 offset1:220
	v_pk_fma_f16 v2, v92, v6, v2
	v_pk_fma_f16 v3, v93, v7, v3
	v_pk_fma_f16 v4, v94, v8, v4
	v_pk_fma_f16 v5, v95, v9, v5
	v_cndmask_b32_e64 v28, v28, v20, s[64:65]
	s_waitcnt lgkmcnt(5)
	v_pk_fma_f16 v6, v2, v144, v145 op_sel:[0,1,1] op_sel_hi:[1,1,1] neg_lo:[1,0,0] neg_hi:[1,0,0]
	v_pk_fma_f16 v7, v3, v144, v145 op_sel:[0,1,1] op_sel_hi:[1,1,1] neg_lo:[1,0,0] neg_hi:[1,0,0]
	v_pk_fma_f16 v8, v4, v144, v145 op_sel:[0,1,1] op_sel_hi:[1,1,1] neg_lo:[1,0,0] neg_hi:[1,0,0]
	v_pk_fma_f16 v9, v5, v144, v145 op_sel:[0,1,1] op_sel_hi:[1,1,1] neg_lo:[1,0,0] neg_hi:[1,0,0]
	v_mfma_f32_16x16x32_f16 v[18:21], v[10:13], v[2:5], 0
	ds_read2_b64 v[60:63], v32 offset0:19 offset1:221
	ds_read_b128 v[124:127], v33 offset:144
	v_pk_fma_f16 v2, v96, v6, v2
	v_pk_fma_f16 v3, v97, v7, v3
	v_pk_fma_f16 v4, v98, v8, v4
	v_pk_fma_f16 v5, v99, v9, v5
	v_cndmask_b32_e64 v29, v29, v25, s[64:65]
	s_cmp_eq_u32 s72, 1
	s_cbranch_scc0 .Lc1_ns0
	s_waitcnt lgkmcnt(7)
	v_readfirstlane_b32 s4, v45
	s_cmp_eq_u32 s4, 4
	s_cbranch_scc0 .Lc1_dslow0

.Lc1_ns0:
	v_pk_fma_f16 v6, v2, v146, v147 op_sel:[0,1,1] op_sel_hi:[1,1,1] neg_lo:[1,0,0] neg_hi:[1,0,0]
	v_pk_fma_f16 v7, v3, v146, v147 op_sel:[0,1,1] op_sel_hi:[1,1,1] neg_lo:[1,0,0] neg_hi:[1,0,0]
	v_pk_fma_f16 v8, v4, v146, v147 op_sel:[0,1,1] op_sel_hi:[1,1,1] neg_lo:[1,0,0] neg_hi:[1,0,0]
	v_pk_fma_f16 v9, v5, v146, v147 op_sel:[0,1,1] op_sel_hi:[1,1,1] neg_lo:[1,0,0] neg_hi:[1,0,0]
	v_mfma_f32_16x16x32_f16 v[22:25], v[10:13], v[2:5], 0
	ds_read2_b64 v[64:67], v32 offset0:20 offset1:222
	v_pk_fma_f16 v2, v100, v6, v2
	v_pk_fma_f16 v3, v101, v7, v3
	v_pk_fma_f16 v4, v102, v8, v4
	v_pk_fma_f16 v5, v103, v9, v5
	v_cndmask_b32_e64 v26, v26, v18, s[66:67]
	v_pk_fma_f16 v6, v2, v148, v149 op_sel:[0,1,1] op_sel_hi:[1,1,1] neg_lo:[1,0,0] neg_hi:[1,0,0]
	v_pk_fma_f16 v7, v3, v148, v149 op_sel:[0,1,1] op_sel_hi:[1,1,1] neg_lo:[1,0,0] neg_hi:[1,0,0]
	v_pk_fma_f16 v8, v4, v148, v149 op_sel:[0,1,1] op_sel_hi:[1,1,1] neg_lo:[1,0,0] neg_hi:[1,0,0]
	v_pk_fma_f16 v9, v5, v148, v149 op_sel:[0,1,1] op_sel_hi:[1,1,1] neg_lo:[1,0,0] neg_hi:[1,0,0]
	v_mfma_f32_16x16x32_f16 v[18:21], v[10:13], v[2:5], 0
	ds_read2_b64 v[68:71], v32 offset0:21 offset1:223
	ds_read_b128 v[128:131], v33 offset:160
	v_pk_fma_f16 v2, v104, v6, v2
	v_pk_fma_f16 v3, v105, v7, v3
	v_pk_fma_f16 v4, v106, v8, v4
	v_pk_fma_f16 v5, v107, v9, v5
	v_cndmask_b32_e64 v27, v27, v23, s[66:67]
	v_pk_fma_f16 v6, v2, v150, v151 op_sel:[0,1,1] op_sel_hi:[1,1,1] neg_lo:[1,0,0] neg_hi:[1,0,0]
	v_pk_fma_f16 v7, v3, v150, v151 op_sel:[0,1,1] op_sel_hi:[1,1,1] neg_lo:[1,0,0] neg_hi:[1,0,0]
	v_pk_fma_f16 v8, v4, v150, v151 op_sel:[0,1,1] op_sel_hi:[1,1,1] neg_lo:[1,0,0] neg_hi:[1,0,0]
	v_pk_fma_f16 v9, v5, v150, v151 op_sel:[0,1,1] op_sel_hi:[1,1,1] neg_lo:[1,0,0] neg_hi:[1,0,0]
	v_mfma_f32_16x16x32_f16 v[22:25], v[10:13], v[2:5], 0
	ds_read2_b64 v[72:75], v32 offset0:22 offset1:224
	v_pk_fma_f16 v2, v108, v6, v2
	v_pk_fma_f16 v3, v109, v7, v3
	v_pk_fma_f16 v4, v110, v8, v4
	v_pk_fma_f16 v5, v111, v9, v5
	v_cndmask_b32_e64 v28, v28, v20, s[66:67]
.Lc1_next0:
	s_waitcnt lgkmcnt(4)
	v_pk_fma_f16 v6, v2, v120, v121 op_sel:[0,1,1] op_sel_hi:[1,1,1] neg_lo:[1,0,0] neg_hi:[1,0,0]
	v_pk_fma_f16 v7, v3, v120, v121 op_sel:[0,1,1] op_sel_hi:[1,1,1] neg_lo:[1,0,0] neg_hi:[1,0,0]
	v_pk_fma_f16 v8, v4, v120, v121 op_sel:[0,1,1] op_sel_hi:[1,1,1] neg_lo:[1,0,0] neg_hi:[1,0,0]
	v_pk_fma_f16 v9, v5, v120, v121 op_sel:[0,1,1] op_sel_hi:[1,1,1] neg_lo:[1,0,0] neg_hi:[1,0,0]
	v_mfma_f32_16x16x32_f16 v[18:21], v[14:17], v[2:5], 0
	ds_read2_b64 v[76:79], v32 offset0:23 offset1:225
	ds_read_b128 v[132:135], v33 offset:176
	ds_read_b32 v37, v36 offset:8
	ds_read_b32 v38, v36 offset:72
	v_pk_fma_f16 v2, v48, v6, v2
	v_pk_fma_f16 v3, v49, v7, v3
	v_pk_fma_f16 v4, v50, v8, v4
	v_pk_fma_f16 v5, v51, v9, v5
	v_cndmask_b32_e64 v29, v29, v25, s[66:67]
	v_cvt_pk_f16_f32 v30, v26, v27
	v_cvt_pk_f16_f32 v31, v28, v29
	ds_write_b16 v39, v30 offset:2048
	ds_write_b16_d16_hi v39, v30 offset:2112
	ds_write_b16 v39, v31 offset:2176
	ds_write_b16_d16_hi v39, v31 offset:2240
	s_mov_b64 exec, 1
	ds_add_u32 v36, v44 offset:128
	s_mov_b64 exec, -1
	v_pk_fma_f16 v6, v2, v122, v123 op_sel:[0,1,1] op_sel_hi:[1,1,1] neg_lo:[1,0,0] neg_hi:[1,0,0]
	v_pk_fma_f16 v7, v3, v122, v123 op_sel:[0,1,1] op_sel_hi:[1,1,1] neg_lo:[1,0,0] neg_hi:[1,0,0]
	v_pk_fma_f16 v8, v4, v122, v123 op_sel:[0,1,1] op_sel_hi:[1,1,1] neg_lo:[1,0,0] neg_hi:[1,0,0]
	v_pk_fma_f16 v9, v5, v122, v123 op_sel:[0,1,1] op_sel_hi:[1,1,1] neg_lo:[1,0,0] neg_hi:[1,0,0]
	v_mfma_f32_16x16x32_f16 v[22:25], v[14:17], v[2:5], 0
	ds_read2_b64 v[80:83], v32 offset0:24 offset1:226
	v_pk_fma_f16 v2, v52, v6, v2
	v_pk_fma_f16 v3, v53, v7, v3
	v_pk_fma_f16 v4, v54, v8, v4
	v_pk_fma_f16 v5, v55, v9, v5
	v_cndmask_b32_e64 v26, v26, v18, s[60:61]
	v_pk_fma_f16 v6, v2, v124, v125 op_sel:[0,1,1] op_sel_hi:[1,1,1] neg_lo:[1,0,0] neg_hi:[1,0,0]
	v_pk_fma_f16 v7, v3, v124, v125 op_sel:[0,1,1] op_sel_hi:[1,1,1] neg_lo:[1,0,0] neg_hi:[1,0,0]
	v_pk_fma_f16 v8, v4, v124, v125 op_sel:[0,1,1] op_sel_hi:[1,1,1] neg_lo:[1,0,0] neg_hi:[1,0,0]
	v_pk_fma_f16 v9, v5, v124, v125 op_sel:[0,1,1] op_sel_hi:[1,1,1] neg_lo:[1,0,0] neg_hi:[1,0,0]
	v_mfma_f32_16x16x32_f16 v[18:21], v[14:17], v[2:5], 0
	ds_read2_b64 v[84:87], v32 offset0:25 offset1:227
	ds_read_b128 v[136:139], v33 offset:192
	v_pk_fma_f16 v2, v56, v6, v2
	v_pk_fma_f16 v3, v57, v7, v3
	v_pk_fma_f16 v4, v58, v8, v4
	v_pk_fma_f16 v5, v59, v9, v5
	v_cndmask_b32_e64 v27, v27, v23, s[60:61]
	v_pk_fma_f16 v6, v2, v126, v127 op_sel:[0,1,1] op_sel_hi:[1,1,1] neg_lo:[1,0,0] neg_hi:[1,0,0]
	v_pk_fma_f16 v7, v3, v126, v127 op_sel:[0,1,1] op_sel_hi:[1,1,1] neg_lo:[1,0,0] neg_hi:[1,0,0]
	v_pk_fma_f16 v8, v4, v126, v127 op_sel:[0,1,1] op_sel_hi:[1,1,1] neg_lo:[1,0,0] neg_hi:[1,0,0]
	v_pk_fma_f16 v9, v5, v126, v127 op_sel:[0,1,1] op_sel_hi:[1,1,1] neg_lo:[1,0,0] neg_hi:[1,0,0]
	v_mfma_f32_16x16x32_f16 v[22:25], v[14:17], v[2:5], 0
	ds_read2_b64 v[88:91], v32 offset0:26 offset1:228
	v_pk_fma_f16 v2, v60, v6, v2
	v_pk_fma_f16 v3, v61, v7, v3
	v_pk_fma_f16 v4, v62, v8, v4
	v_pk_fma_f16 v5, v63, v9, v5
	v_cndmask_b32_e64 v28, v28, v20, s[60:61]
	s_waitcnt lgkmcnt(11)
	v_pk_fma_f16 v6, v2, v128, v129 op_sel:[0,1,1] op_sel_hi:[1,1,1] neg_lo:[1,0,0] neg_hi:[1,0,0]
	v_pk_fma_f16 v7, v3, v128, v129 op_sel:[0,1,1] op_sel_hi:[1,1,1] neg_lo:[1,0,0] neg_hi:[1,0,0]
	v_pk_fma_f16 v8, v4, v128, v129 op_sel:[0,1,1] op_sel_hi:[1,1,1] neg_lo:[1,0,0] neg_hi:[1,0,0]
	v_pk_fma_f16 v9, v5, v128, v129 op_sel:[0,1,1] op_sel_hi:[1,1,1] neg_lo:[1,0,0] neg_hi:[1,0,0]
	v_mfma_f32_16x16x32_f16 v[18:21], v[14:17], v[2:5], 0
	ds_read2_b64 v[92:95], v32 offset0:27 offset1:229
	ds_read_b128 v[140:143], v33 offset:208
	v_pk_fma_f16 v2, v64, v6, v2
	v_pk_fma_f16 v3, v65, v7, v3
	v_pk_fma_f16 v4, v66, v8, v4
	v_pk_fma_f16 v5, v67, v9, v5
	v_cndmask_b32_e64 v29, v29, v25, s[60:61]
	v_pk_fma_f16 v6, v2, v130, v131 op_sel:[0,1,1] op_sel_hi:[1,1,1] neg_lo:[1,0,0] neg_hi:[1,0,0]
	v_pk_fma_f16 v7, v3, v130, v131 op_sel:[0,1,1] op_sel_hi:[1,1,1] neg_lo:[1,0,0] neg_hi:[1,0,0]
	v_pk_fma_f16 v8, v4, v130, v131 op_sel:[0,1,1] op_sel_hi:[1,1,1] neg_lo:[1,0,0] neg_hi:[1,0,0]
	v_pk_fma_f16 v9, v5, v130, v131 op_sel:[0,1,1] op_sel_hi:[1,1,1] neg_lo:[1,0,0] neg_hi:[1,0,0]
	v_mfma_f32_16x16x32_f16 v[22:25], v[14:17], v[2:5], 0
	ds_read2_b64 v[96:99], v32 offset0:28 offset1:230
	v_pk_fma_f16 v2, v68, v6, v2
	v_pk_fma_f16 v3, v69, v7, v3
	v_pk_fma_f16 v4, v70, v8, v4
	v_pk_fma_f16 v5, v71, v9, v5
	v_cndmask_b32_e64 v26, v26, v18, s[62:63]
	v_pk_fma_f16 v6, v2, v132, v133 op_sel:[0,1,1] op_sel_hi:[1,1,1] neg_lo:[1,0,0] neg_hi:[1,0,0]
	v_pk_fma_f16 v7, v3, v132, v133 op_sel:[0,1,1] op_sel_hi:[1,1,1] neg_lo:[1,0,0] neg_hi:[1,0,0]
	v_pk_fma_f16 v8, v4, v132, v133 op_sel:[0,1,1] op_sel_hi:[1,1,1] neg_lo:[1,0,0] neg_hi:[1,0,0]
	v_pk_fma_f16 v9, v5, v132, v133 op_sel:[0,1,1] op_sel_hi:[1,1,1] neg_lo:[1,0,0] neg_hi:[1,0,0]
	v_mfma_f32_16x16x32_f16 v[18:21], v[14:17], v[2:5], 0
	ds_read2_b64 v[100:103], v32 offset0:29 offset1:231
	ds_read_b128 v[144:147], v33 offset:224
	v_pk_fma_f16 v2, v72, v6, v2
	v_pk_fma_f16 v3, v73, v7, v3
	v_pk_fma_f16 v4, v74, v8, v4
	v_pk_fma_f16 v5, v75, v9, v5
	v_cndmask_b32_e64 v27, v27, v23, s[62:63]
	v_pk_fma_f16 v6, v2, v134, v135 op_sel:[0,1,1] op_sel_hi:[1,1,1] neg_lo:[1,0,0] neg_hi:[1,0,0]
	v_pk_fma_f16 v7, v3, v134, v135 op_sel:[0,1,1] op_sel_hi:[1,1,1] neg_lo:[1,0,0] neg_hi:[1,0,0]
	v_pk_fma_f16 v8, v4, v134, v135 op_sel:[0,1,1] op_sel_hi:[1,1,1] neg_lo:[1,0,0] neg_hi:[1,0,0]
	v_pk_fma_f16 v9, v5, v134, v135 op_sel:[0,1,1] op_sel_hi:[1,1,1] neg_lo:[1,0,0] neg_hi:[1,0,0]
	v_mfma_f32_16x16x32_f16 v[22:25], v[14:17], v[2:5], 0
	ds_read2_b64 v[104:107], v32 offset0:30 offset1:232
	v_pk_fma_f16 v2, v76, v6, v2
	v_pk_fma_f16 v3, v77, v7, v3
	v_pk_fma_f16 v4, v78, v8, v4
	v_pk_fma_f16 v5, v79, v9, v5
	v_cndmask_b32_e64 v28, v28, v20, s[62:63]
	s_waitcnt lgkmcnt(4)
	v_pk_fma_f16 v6, v2, v136, v137 op_sel:[0,1,1] op_sel_hi:[1,1,1] neg_lo:[1,0,0] neg_hi:[1,0,0]
	v_pk_fma_f16 v7, v3, v136, v137 op_sel:[0,1,1] op_sel_hi:[1,1,1] neg_lo:[1,0,0] neg_hi:[1,0,0]
	v_pk_fma_f16 v8, v4, v136, v137 op_sel:[0,1,1] op_sel_hi:[1,1,1] neg_lo:[1,0,0] neg_hi:[1,0,0]
	v_pk_fma_f16 v9, v5, v136, v137 op_sel:[0,1,1] op_sel_hi:[1,1,1] neg_lo:[1,0,0] neg_hi:[1,0,0]
	v_mfma_f32_16x16x32_f16 v[18:21], v[14:17], v[2:5], 0
	ds_read2_b64 v[108:111], v32 offset0:31 offset1:233
	ds_read_b128 v[148:151], v33 offset:240
	v_pk_fma_f16 v2, v80, v6, v2
	v_pk_fma_f16 v3, v81, v7, v3
	v_pk_fma_f16 v4, v82, v8, v4
	v_pk_fma_f16 v5, v83, v9, v5
	v_cndmask_b32_e64 v29, v29, v25, s[62:63]
	v_readfirstlane_b32 s4, v37
	v_readfirstlane_b32 s5, v38
	s_and_b32 s4, s4, s5
	s_cbranch_scc0 .Lc1_slow1

.Lc1_nd1:
	v_pk_fma_f16 v6, v2, v138, v139 op_sel:[0,1,1] op_sel_hi:[1,1,1] neg_lo:[1,0,0] neg_hi:[1,0,0]
	v_pk_fma_f16 v7, v3, v138, v139 op_sel:[0,1,1] op_sel_hi:[1,1,1] neg_lo:[1,0,0] neg_hi:[1,0,0]
	v_pk_fma_f16 v8, v4, v138, v139 op_sel:[0,1,1] op_sel_hi:[1,1,1] neg_lo:[1,0,0] neg_hi:[1,0,0]
	v_pk_fma_f16 v9, v5, v138, v139 op_sel:[0,1,1] op_sel_hi:[1,1,1] neg_lo:[1,0,0] neg_hi:[1,0,0]
	v_mfma_f32_16x16x32_f16 v[22:25], v[14:17], v[2:5], 0
	ds_read2_b64 v[48:51], v32 offset0:32 offset1:234
	v_pk_fma_f16 v2, v84, v6, v2
	v_pk_fma_f16 v3, v85, v7, v3
	v_pk_fma_f16 v4, v86, v8, v4
	v_pk_fma_f16 v5, v87, v9, v5
	v_cndmask_b32_e64 v26, v26, v18, s[64:65]
	v_pk_fma_f16 v6, v2, v140, v141 op_sel:[0,1,1] op_sel_hi:[1,1,1] neg_lo:[1,0,0] neg_hi:[1,0,0]
	v_pk_fma_f16 v7, v3, v140, v141 op_sel:[0,1,1] op_sel_hi:[1,1,1] neg_lo:[1,0,0] neg_hi:[1,0,0]
	v_pk_fma_f16 v8, v4, v140, v141 op_sel:[0,1,1] op_sel_hi:[1,1,1] neg_lo:[1,0,0] neg_hi:[1,0,0]
	v_pk_fma_f16 v9, v5, v140, v141 op_sel:[0,1,1] op_sel_hi:[1,1,1] neg_lo:[1,0,0] neg_hi:[1,0,0]
	v_mfma_f32_16x16x32_f16 v[18:21], v[14:17], v[2:5], 0
	ds_read2_b64 v[52:55], v32 offset0:33 offset1:235
	ds_read_b128 v[120:123], v33 offset:256
	ds_read2_b64 v[10:13], v34 offset0:32 offset1:234
	v_pk_fma_f16 v2, v88, v6, v2
	v_pk_fma_f16 v3, v89, v7, v3
	v_pk_fma_f16 v4, v90, v8, v4
	v_pk_fma_f16 v5, v91, v9, v5
	v_cndmask_b32_e64 v27, v27, v23, s[64:65]
	v_pk_fma_f16 v6, v2, v142, v143 op_sel:[0,1,1] op_sel_hi:[1,1,1] neg_lo:[1,0,0] neg_hi:[1,0,0]
	v_pk_fma_f16 v7, v3, v142, v143 op_sel:[0,1,1] op_sel_hi:[1,1,1] neg_lo:[1,0,0] neg_hi:[1,0,0]
	v_pk_fma_f16 v8, v4, v142, v143 op_sel:[0,1,1] op_sel_hi:[1,1,1] neg_lo:[1,0,0] neg_hi:[1,0,0]
	v_pk_fma_f16 v9, v5, v142, v143 op_sel:[0,1,1] op_sel_hi:[1,1,1] neg_lo:[1,0,0] neg_hi:[1,0,0]
	v_mfma_f32_16x16x32_f16 v[22:25], v[14:17], v[2:5], 0
	ds_read2_b64 v[56:59], v32 offset0:34 offset1:236
	v_pk_fma_f16 v2, v92, v6, v2
	v_pk_fma_f16 v3, v93, v7, v3
	v_pk_fma_f16 v4, v94, v8, v4
	v_pk_fma_f16 v5, v95, v9, v5
	v_cndmask_b32_e64 v28, v28, v20, s[64:65]
	s_waitcnt lgkmcnt(5)
	v_pk_fma_f16 v6, v2, v144, v145 op_sel:[0,1,1] op_sel_hi:[1,1,1] neg_lo:[1,0,0] neg_hi:[1,0,0]
	v_pk_fma_f16 v7, v3, v144, v145 op_sel:[0,1,1] op_sel_hi:[1,1,1] neg_lo:[1,0,0] neg_hi:[1,0,0]
	v_pk_fma_f16 v8, v4, v144, v145 op_sel:[0,1,1] op_sel_hi:[1,1,1] neg_lo:[1,0,0] neg_hi:[1,0,0]
	v_pk_fma_f16 v9, v5, v144, v145 op_sel:[0,1,1] op_sel_hi:[1,1,1] neg_lo:[1,0,0] neg_hi:[1,0,0]
	v_mfma_f32_16x16x32_f16 v[18:21], v[14:17], v[2:5], 0
	ds_read2_b64 v[60:63], v32 offset0:35 offset1:237
	ds_read_b128 v[124:127], v33 offset:272
	v_pk_fma_f16 v2, v96, v6, v2
	v_pk_fma_f16 v3, v97, v7, v3
	v_pk_fma_f16 v4, v98, v8, v4
	v_pk_fma_f16 v5, v99, v9, v5
	v_cndmask_b32_e64 v29, v29, v25, s[64:65]
	s_cmp_eq_u32 s72, 1
	s_cbranch_scc0 .Lc1_ns1
	s_waitcnt lgkmcnt(7)
	v_readfirstlane_b32 s4, v45
	s_cmp_eq_u32 s4, 4
	s_cbranch_scc0 .Lc1_dslow1

.Lc1_ns1:
	v_pk_fma_f16 v6, v2, v146, v147 op_sel:[0,1,1] op_sel_hi:[1,1,1] neg_lo:[1,0,0] neg_hi:[1,0,0]
	v_pk_fma_f16 v7, v3, v146, v147 op_sel:[0,1,1] op_sel_hi:[1,1,1] neg_lo:[1,0,0] neg_hi:[1,0,0]
	v_pk_fma_f16 v8, v4, v146, v147 op_sel:[0,1,1] op_sel_hi:[1,1,1] neg_lo:[1,0,0] neg_hi:[1,0,0]
	v_pk_fma_f16 v9, v5, v146, v147 op_sel:[0,1,1] op_sel_hi:[1,1,1] neg_lo:[1,0,0] neg_hi:[1,0,0]
	v_mfma_f32_16x16x32_f16 v[22:25], v[14:17], v[2:5], 0
	ds_read2_b64 v[64:67], v32 offset0:36 offset1:238
	v_pk_fma_f16 v2, v100, v6, v2
	v_pk_fma_f16 v3, v101, v7, v3
	v_pk_fma_f16 v4, v102, v8, v4
	v_pk_fma_f16 v5, v103, v9, v5
	v_cndmask_b32_e64 v26, v26, v18, s[66:67]
	v_pk_fma_f16 v6, v2, v148, v149 op_sel:[0,1,1] op_sel_hi:[1,1,1] neg_lo:[1,0,0] neg_hi:[1,0,0]
	v_pk_fma_f16 v7, v3, v148, v149 op_sel:[0,1,1] op_sel_hi:[1,1,1] neg_lo:[1,0,0] neg_hi:[1,0,0]
	v_pk_fma_f16 v8, v4, v148, v149 op_sel:[0,1,1] op_sel_hi:[1,1,1] neg_lo:[1,0,0] neg_hi:[1,0,0]
	v_pk_fma_f16 v9, v5, v148, v149 op_sel:[0,1,1] op_sel_hi:[1,1,1] neg_lo:[1,0,0] neg_hi:[1,0,0]
	v_mfma_f32_16x16x32_f16 v[18:21], v[14:17], v[2:5], 0
	ds_read2_b64 v[68:71], v32 offset0:37 offset1:239
	ds_read_b128 v[128:131], v33 offset:288
	v_pk_fma_f16 v2, v104, v6, v2
	v_pk_fma_f16 v3, v105, v7, v3
	v_pk_fma_f16 v4, v106, v8, v4
	v_pk_fma_f16 v5, v107, v9, v5
	v_cndmask_b32_e64 v27, v27, v23, s[66:67]
	v_pk_fma_f16 v6, v2, v150, v151 op_sel:[0,1,1] op_sel_hi:[1,1,1] neg_lo:[1,0,0] neg_hi:[1,0,0]
	v_pk_fma_f16 v7, v3, v150, v151 op_sel:[0,1,1] op_sel_hi:[1,1,1] neg_lo:[1,0,0] neg_hi:[1,0,0]
	v_pk_fma_f16 v8, v4, v150, v151 op_sel:[0,1,1] op_sel_hi:[1,1,1] neg_lo:[1,0,0] neg_hi:[1,0,0]
	v_pk_fma_f16 v9, v5, v150, v151 op_sel:[0,1,1] op_sel_hi:[1,1,1] neg_lo:[1,0,0] neg_hi:[1,0,0]
	v_mfma_f32_16x16x32_f16 v[22:25], v[14:17], v[2:5], 0
	ds_read2_b64 v[72:75], v32 offset0:38 offset1:240
	v_pk_fma_f16 v2, v108, v6, v2
	v_pk_fma_f16 v3, v109, v7, v3
	v_pk_fma_f16 v4, v110, v8, v4
	v_pk_fma_f16 v5, v111, v9, v5
	v_cndmask_b32_e64 v28, v28, v20, s[66:67]
.Lc1_next1:
	v_add_u32_e32 v32, 0x100, v32
	v_add_u32_e32 v33, 0x100, v33
	v_add_u32_e32 v34, 0x100, v34
	v_add_u32_e32 v36, 8, v36
	v_add_u32_e32 v39, 0x1000, v39
	v_add_u32_e32 v43, 0x1000, v43
	v_add_u32_e32 v35, 0x800, v35
	s_xor_b32 s71, s71, 2
	s_add_i32 s70, s70, 1
	s_cmp_lt_u32 s70, 6
	s_cbranch_scc1 .Lc1_loop
	s_waitcnt lgkmcnt(4)
	v_pk_fma_f16 v6, v2, v120, v121 op_sel:[0,1,1] op_sel_hi:[1,1,1] neg_lo:[1,0,0] neg_hi:[1,0,0]
	v_pk_fma_f16 v7, v3, v120, v121 op_sel:[0,1,1] op_sel_hi:[1,1,1] neg_lo:[1,0,0] neg_hi:[1,0,0]
	v_pk_fma_f16 v8, v4, v120, v121 op_sel:[0,1,1] op_sel_hi:[1,1,1] neg_lo:[1,0,0] neg_hi:[1,0,0]
	v_pk_fma_f16 v9, v5, v120, v121 op_sel:[0,1,1] op_sel_hi:[1,1,1] neg_lo:[1,0,0] neg_hi:[1,0,0]
	v_mfma_f32_16x16x32_f16 v[18:21], v[10:13], v[2:5], 0
	ds_read2_b64 v[76:79], v32 offset0:7 offset1:209
	ds_read_b128 v[132:135], v33 offset:48
	v_pk_fma_f16 v2, v48, v6, v2
	v_pk_fma_f16 v3, v49, v7, v3
	v_pk_fma_f16 v4, v50, v8, v4
	v_pk_fma_f16 v5, v51, v9, v5
	v_cndmask_b32_e64 v29, v29, v25, s[66:67]
	v_cvt_pk_f16_f32 v30, v26, v27
	v_cvt_pk_f16_f32 v31, v28, v29
	ds_write_b16 v39, v30 offset:0
	ds_write_b16_d16_hi v39, v30 offset:64
	ds_write_b16 v39, v31 offset:128
	ds_write_b16_d16_hi v39, v31 offset:192
	s_mov_b64 exec, 1
	ds_add_u32 v36, v44 offset:124
	s_mov_b64 exec, -1
	v_pk_fma_f16 v6, v2, v122, v123 op_sel:[0,1,1] op_sel_hi:[1,1,1] neg_lo:[1,0,0] neg_hi:[1,0,0]
	v_pk_fma_f16 v7, v3, v122, v123 op_sel:[0,1,1] op_sel_hi:[1,1,1] neg_lo:[1,0,0] neg_hi:[1,0,0]
	v_pk_fma_f16 v8, v4, v122, v123 op_sel:[0,1,1] op_sel_hi:[1,1,1] neg_lo:[1,0,0] neg_hi:[1,0,0]
	v_pk_fma_f16 v9, v5, v122, v123 op_sel:[0,1,1] op_sel_hi:[1,1,1] neg_lo:[1,0,0] neg_hi:[1,0,0]
	v_mfma_f32_16x16x32_f16 v[22:25], v[10:13], v[2:5], 0
	v_pk_fma_f16 v2, v52, v6, v2
	v_pk_fma_f16 v3, v53, v7, v3
	v_pk_fma_f16 v4, v54, v8, v4
	v_pk_fma_f16 v5, v55, v9, v5
	v_cndmask_b32_e64 v26, v26, v18, s[60:61]
	v_pk_fma_f16 v6, v2, v124, v125 op_sel:[0,1,1] op_sel_hi:[1,1,1] neg_lo:[1,0,0] neg_hi:[1,0,0]
	v_pk_fma_f16 v7, v3, v124, v125 op_sel:[0,1,1] op_sel_hi:[1,1,1] neg_lo:[1,0,0] neg_hi:[1,0,0]
	v_pk_fma_f16 v8, v4, v124, v125 op_sel:[0,1,1] op_sel_hi:[1,1,1] neg_lo:[1,0,0] neg_hi:[1,0,0]
	v_pk_fma_f16 v9, v5, v124, v125 op_sel:[0,1,1] op_sel_hi:[1,1,1] neg_lo:[1,0,0] neg_hi:[1,0,0]
	v_mfma_f32_16x16x32_f16 v[18:21], v[10:13], v[2:5], 0
	v_pk_fma_f16 v2, v56, v6, v2
	v_pk_fma_f16 v3, v57, v7, v3
	v_pk_fma_f16 v4, v58, v8, v4
	v_pk_fma_f16 v5, v59, v9, v5
	v_cndmask_b32_e64 v27, v27, v23, s[60:61]
	v_pk_fma_f16 v6, v2, v126, v127 op_sel:[0,1,1] op_sel_hi:[1,1,1] neg_lo:[1,0,0] neg_hi:[1,0,0]
	v_pk_fma_f16 v7, v3, v126, v127 op_sel:[0,1,1] op_sel_hi:[1,1,1] neg_lo:[1,0,0] neg_hi:[1,0,0]
	v_pk_fma_f16 v8, v4, v126, v127 op_sel:[0,1,1] op_sel_hi:[1,1,1] neg_lo:[1,0,0] neg_hi:[1,0,0]
	v_pk_fma_f16 v9, v5, v126, v127 op_sel:[0,1,1] op_sel_hi:[1,1,1] neg_lo:[1,0,0] neg_hi:[1,0,0]
	v_mfma_f32_16x16x32_f16 v[22:25], v[10:13], v[2:5], 0
	v_pk_fma_f16 v2, v60, v6, v2
	v_pk_fma_f16 v3, v61, v7, v3
	v_pk_fma_f16 v4, v62, v8, v4
	v_pk_fma_f16 v5, v63, v9, v5
	v_cndmask_b32_e64 v28, v28, v20, s[60:61]
	s_waitcnt lgkmcnt(5)
	s_mov_b32 s72, 0
	s_cmp_eq_u32 s70, 0
	s_cbranch_scc1 .Lc1_ndt
	s_cmp_eq_u32 s36, 3
	s_cbranch_scc0 .Lc1_ndt
	s_mov_b32 s72, 1
	ds_read_b32 v45, v36 offset:124
	ds_read_b128 v[112:115], v43 offset:0
	ds_read_b128 v[116:119], v43 offset:1024
.Lc1_ndt:
	v_pk_fma_f16 v6, v2, v128, v129 op_sel:[0,1,1] op_sel_hi:[1,1,1] neg_lo:[1,0,0] neg_hi:[1,0,0]
	v_pk_fma_f16 v7, v3, v128, v129 op_sel:[0,1,1] op_sel_hi:[1,1,1] neg_lo:[1,0,0] neg_hi:[1,0,0]
	v_pk_fma_f16 v8, v4, v128, v129 op_sel:[0,1,1] op_sel_hi:[1,1,1] neg_lo:[1,0,0] neg_hi:[1,0,0]
	v_pk_fma_f16 v9, v5, v128, v129 op_sel:[0,1,1] op_sel_hi:[1,1,1] neg_lo:[1,0,0] neg_hi:[1,0,0]
	v_mfma_f32_16x16x32_f16 v[18:21], v[10:13], v[2:5], 0
	v_pk_fma_f16 v2, v64, v6, v2
	v_pk_fma_f16 v3, v65, v7, v3
	v_pk_fma_f16 v4, v66, v8, v4
	v_pk_fma_f16 v5, v67, v9, v5
	v_cndmask_b32_e64 v29, v29, v25, s[60:61]
	v_pk_fma_f16 v6, v2, v130, v131 op_sel:[0,1,1] op_sel_hi:[1,1,1] neg_lo:[1,0,0] neg_hi:[1,0,0]
	v_pk_fma_f16 v7, v3, v130, v131 op_sel:[0,1,1] op_sel_hi:[1,1,1] neg_lo:[1,0,0] neg_hi:[1,0,0]
	v_pk_fma_f16 v8, v4, v130, v131 op_sel:[0,1,1] op_sel_hi:[1,1,1] neg_lo:[1,0,0] neg_hi:[1,0,0]
	v_pk_fma_f16 v9, v5, v130, v131 op_sel:[0,1,1] op_sel_hi:[1,1,1] neg_lo:[1,0,0] neg_hi:[1,0,0]
	v_mfma_f32_16x16x32_f16 v[22:25], v[10:13], v[2:5], 0
	v_pk_fma_f16 v2, v68, v6, v2
	v_pk_fma_f16 v3, v69, v7, v3
	v_pk_fma_f16 v4, v70, v8, v4
	v_pk_fma_f16 v5, v71, v9, v5
	v_cndmask_b32_e64 v26, v26, v18, s[62:63]
	v_pk_fma_f16 v6, v2, v132, v133 op_sel:[0,1,1] op_sel_hi:[1,1,1] neg_lo:[1,0,0] neg_hi:[1,0,0]
	v_pk_fma_f16 v7, v3, v132, v133 op_sel:[0,1,1] op_sel_hi:[1,1,1] neg_lo:[1,0,0] neg_hi:[1,0,0]
	v_pk_fma_f16 v8, v4, v132, v133 op_sel:[0,1,1] op_sel_hi:[1,1,1] neg_lo:[1,0,0] neg_hi:[1,0,0]
	v_pk_fma_f16 v9, v5, v132, v133 op_sel:[0,1,1] op_sel_hi:[1,1,1] neg_lo:[1,0,0] neg_hi:[1,0,0]
	v_mfma_f32_16x16x32_f16 v[18:21], v[10:13], v[2:5], 0
	v_pk_fma_f16 v2, v72, v6, v2
	v_pk_fma_f16 v3, v73, v7, v3
	v_pk_fma_f16 v4, v74, v8, v4
	v_pk_fma_f16 v5, v75, v9, v5
	v_cndmask_b32_e64 v27, v27, v23, s[62:63]
	s_cmp_eq_u32 s72, 1
	s_cbranch_scc0 .Lc1_nst
	s_waitcnt lgkmcnt(0)
	v_readfirstlane_b32 s4, v45
	s_cmp_eq_u32 s4, 4
	s_cbranch_scc0 .Lc1_dslowt
